# pass A: two partial FMA chains per table row (even and odd bytes) so dependent FMAs sit eight instructions apart, summed at the end of the row
# speedup vs baseline: 1.0057x; 1.0003x over previous
.Lpa_tok:
	v_lshlrev_b32_e32 v124, 16, v116
	v_and_b32_e32 v125, 0xffff0000, v116
	v_pk_mul_f32 v[108:109], v[124:125], v[100:101]
	v_lshlrev_b32_e32 v124, 16, v117
	v_and_b32_e32 v125, 0xffff0000, v117
	v_pk_mul_f32 v[110:111], v[124:125], v[102:103]
	v_lshlrev_b32_e32 v124, 16, v118
	v_and_b32_e32 v125, 0xffff0000, v118
	v_pk_mul_f32 v[112:113], v[124:125], v[104:105]
	v_lshlrev_b32_e32 v124, 16, v119
	v_and_b32_e32 v125, 0xffff0000, v119
	v_pk_mul_f32 v[114:115], v[124:125], v[106:107]
	v_add_f32_e32 v16, v108, v109
	v_add_f32_e32 v17, v110, v111
	v_add_f32_e32 v18, v112, v113
	v_add_f32_e32 v19, v114, v115
	v_add_f32_e32 v16, v16, v17
	v_add_f32_e32 v18, v18, v19
	v_add_f32_e32 v16, v16, v18
	s_nop 1
	v_add_f32_dpp v17, v16, v16 quad_perm:[1,0,3,2] row_mask:0xf bank_mask:0xf
	s_nop 1
	v_add_f32_dpp v16, v17, v17 quad_perm:[2,3,0,1] row_mask:0xf bank_mask:0xf
	s_nop 1
	v_add_f32_dpp v17, v16, v16 row_half_mirror row_mask:0xf bank_mask:0xf
	s_nop 1
	v_add_f32_dpp v16, v17, v17 row_ror:8 row_mask:0xf bank_mask:0xf
	v_mov_b32_e32 v17, v16
	s_nop 1
	v_permlane16_swap_b32_e32 v16, v17
	v_add_f32_e32 v16, v16, v17
	v_mov_b32_e32 v17, v16
	s_nop 1
	v_permlane32_swap_b32_e32 v16, v17
	v_add_f32_e32 v16, v16, v17
	s_lshl_b32 s30, s16, 7
	s_add_u32 s28, s22, s30
	s_addc_u32 s29, s23, 0
	v_lshlrev_b32_e32 v19, 1, v1
	s_mov_b64 exec, s[2:3]
	global_store_dword v19, v16, s[28:29]
	s_mov_b64 exec, -1
	v_mov_b32_e32 v120, v122
	v_mov_b32_e32 v121, v123
	s_lshl_b32 s30, s16, 9
	v_lshl_add_u64 v[22:23], v[176:177], 0, s[30:31]
	s_add_i32 s18, s16, 1
	s_min_i32 s18, s18, s24
	s_lshl_b32 s30, s16, 9
	s_add_u32 s36, s40, s30
	s_addc_u32 s37, s41, 0
	s_lshl_b32 s30, s18, 9
	s_add_u32 s38, s40, s30
	s_addc_u32 s39, s41, 0
	s_lshl_b32 s30, s18, 13
	v_lshl_add_u64 v[160:161], v[172:173], 0, s[30:31]
	global_load_dwordx4 v[116:119], v[160:161], off
	s_lshl_b32 s30, s18, 9
	v_lshl_add_u64 v[160:161], v[174:175], 0, s[30:31]
	global_load_dword v122, v[160:161], off
	global_load_dword v123, v[160:161], off offset:256
	s_waitcnt vmcnt(31)
	v_cvt_f32_ubyte0_e32 v124, v24
	v_cvt_f32_ubyte1_e32 v126, v24
	v_cvt_f32_ubyte2_e32 v128, v24
	v_cvt_f32_ubyte3_e32 v130, v24
	v_cvt_f32_ubyte0_e32 v132, v25
	v_cvt_f32_ubyte1_e32 v134, v25
	v_cvt_f32_ubyte2_e32 v136, v25
	v_cvt_f32_ubyte3_e32 v138, v25
	s_waitcnt lgkmcnt(0)
	s_load_dwordx16 s[84:99], s[36:37], 0xc0 glc
	s_lshl_b32 s30, s68, 12
	s_add_u32 s28, s26, s30
	s_addc_u32 s29, s27, 0
	global_load_dwordx2 v[24:25], v162, s[28:29]
	v_cvt_f32_ubyte0_e32 v125, v26
	v_cvt_f32_ubyte1_e32 v127, v26
	v_cvt_f32_ubyte2_e32 v129, v26
	v_cvt_f32_ubyte3_e32 v131, v26
	v_cvt_f32_ubyte0_e32 v133, v27
	v_cvt_f32_ubyte1_e32 v135, v27
	v_cvt_f32_ubyte2_e32 v137, v27
	v_cvt_f32_ubyte3_e32 v139, v27
	s_lshl_b32 s30, s69, 12
	s_add_u32 s28, s26, s30
	s_addc_u32 s29, s27, 0
	global_load_dwordx2 v[26:27], v162, s[28:29]
	v_cvt_f32_ubyte0_e32 v140, v28
	v_cvt_f32_ubyte1_e32 v142, v28
	v_cvt_f32_ubyte2_e32 v144, v28
	v_cvt_f32_ubyte3_e32 v146, v28
	v_cvt_f32_ubyte0_e32 v148, v29
	v_cvt_f32_ubyte1_e32 v150, v29
	v_cvt_f32_ubyte2_e32 v152, v29
	v_cvt_f32_ubyte3_e32 v154, v29
	s_lshl_b32 s30, s70, 12
	s_add_u32 s28, s26, s30
	s_addc_u32 s29, s27, 0
	global_load_dwordx2 v[28:29], v162, s[28:29]
	v_cvt_f32_ubyte0_e32 v141, v30
	v_cvt_f32_ubyte1_e32 v143, v30
	v_cvt_f32_ubyte2_e32 v145, v30
	v_cvt_f32_ubyte3_e32 v147, v30
	v_cvt_f32_ubyte0_e32 v149, v31
	v_cvt_f32_ubyte1_e32 v151, v31
	v_cvt_f32_ubyte2_e32 v153, v31
	v_cvt_f32_ubyte3_e32 v155, v31
	s_lshl_b32 s30, s71, 12
	s_add_u32 s28, s26, s30
	s_addc_u32 s29, s27, 0
	global_load_dwordx2 v[30:31], v162, s[28:29]
	v_mul_f32_e32 v178, v124, v108
	v_mul_f32_e32 v179, v125, v108
	v_mul_f32_e32 v180, v140, v108
	v_mul_f32_e32 v181, v141, v108
	v_mul_f32_e32 v156, v126, v109
	v_mul_f32_e32 v157, v127, v109
	v_mul_f32_e32 v158, v142, v109
	v_mul_f32_e32 v159, v143, v109
	v_fmac_f32_e32 v178, v128, v110
	v_fmac_f32_e32 v179, v129, v110
	v_fmac_f32_e32 v180, v144, v110
	v_fmac_f32_e32 v181, v145, v110
	v_fmac_f32_e32 v156, v130, v111
	v_fmac_f32_e32 v157, v131, v111
	v_fmac_f32_e32 v158, v146, v111
	v_fmac_f32_e32 v159, v147, v111
	v_fmac_f32_e32 v178, v132, v112
	v_fmac_f32_e32 v179, v133, v112
	v_fmac_f32_e32 v180, v148, v112
	v_fmac_f32_e32 v181, v149, v112
	v_fmac_f32_e32 v156, v134, v113
	v_fmac_f32_e32 v157, v135, v113
	v_fmac_f32_e32 v158, v150, v113
	v_fmac_f32_e32 v159, v151, v113
	v_fmac_f32_e32 v178, v136, v114
	v_fmac_f32_e32 v179, v137, v114
	v_fmac_f32_e32 v180, v152, v114
	v_fmac_f32_e32 v181, v153, v114
	v_fmac_f32_e32 v156, v138, v115
	v_fmac_f32_e32 v157, v139, v115
	v_fmac_f32_e32 v158, v154, v115
	v_fmac_f32_e32 v159, v155, v115
	v_add_f32_e32 v178, v178, v156
	v_add_f32_e32 v179, v179, v157
	v_add_f32_e32 v180, v180, v158
	v_add_f32_e32 v181, v181, v159
	s_waitcnt vmcnt(31)
	v_cvt_f32_ubyte0_e32 v124, v32
	v_cvt_f32_ubyte1_e32 v126, v32
	v_cvt_f32_ubyte2_e32 v128, v32
	v_cvt_f32_ubyte3_e32 v130, v32
	v_cvt_f32_ubyte0_e32 v132, v33
	v_cvt_f32_ubyte1_e32 v134, v33
	v_cvt_f32_ubyte2_e32 v136, v33
	v_cvt_f32_ubyte3_e32 v138, v33
	s_lshl_b32 s30, s72, 12
	s_add_u32 s28, s26, s30
	s_addc_u32 s29, s27, 0
	global_load_dwordx2 v[32:33], v162, s[28:29]
	v_cvt_f32_ubyte0_e32 v125, v34
	v_cvt_f32_ubyte1_e32 v127, v34
	v_cvt_f32_ubyte2_e32 v129, v34
	v_cvt_f32_ubyte3_e32 v131, v34
	v_cvt_f32_ubyte0_e32 v133, v35
	v_cvt_f32_ubyte1_e32 v135, v35
	v_cvt_f32_ubyte2_e32 v137, v35
	v_cvt_f32_ubyte3_e32 v139, v35
	s_lshl_b32 s30, s73, 12
	s_add_u32 s28, s26, s30
	s_addc_u32 s29, s27, 0
	global_load_dwordx2 v[34:35], v162, s[28:29]
	v_cvt_f32_ubyte0_e32 v140, v36
	v_cvt_f32_ubyte1_e32 v142, v36
	v_cvt_f32_ubyte2_e32 v144, v36
	v_cvt_f32_ubyte3_e32 v146, v36
	v_cvt_f32_ubyte0_e32 v148, v37
	v_cvt_f32_ubyte1_e32 v150, v37
	v_cvt_f32_ubyte2_e32 v152, v37
	v_cvt_f32_ubyte3_e32 v154, v37
	s_lshl_b32 s30, s74, 12
	s_add_u32 s28, s26, s30
	s_addc_u32 s29, s27, 0
	global_load_dwordx2 v[36:37], v162, s[28:29]
	v_cvt_f32_ubyte0_e32 v141, v38
	v_cvt_f32_ubyte1_e32 v143, v38
	v_cvt_f32_ubyte2_e32 v145, v38
	v_cvt_f32_ubyte3_e32 v147, v38
	v_cvt_f32_ubyte0_e32 v149, v39
	v_cvt_f32_ubyte1_e32 v151, v39
	v_cvt_f32_ubyte2_e32 v153, v39
	v_cvt_f32_ubyte3_e32 v155, v39
	s_lshl_b32 s30, s75, 12
	s_add_u32 s28, s26, s30
	s_addc_u32 s29, s27, 0
	global_load_dwordx2 v[38:39], v162, s[28:29]
	v_mul_f32_e32 v182, v124, v108
	v_mul_f32_e32 v183, v125, v108
	v_mul_f32_e32 v184, v140, v108
	v_mul_f32_e32 v185, v141, v108
	v_mul_f32_e32 v156, v126, v109
	v_mul_f32_e32 v157, v127, v109
	v_mul_f32_e32 v158, v142, v109
	v_mul_f32_e32 v159, v143, v109
	v_fmac_f32_e32 v182, v128, v110
	v_fmac_f32_e32 v183, v129, v110
	v_fmac_f32_e32 v184, v144, v110
	v_fmac_f32_e32 v185, v145, v110
	v_fmac_f32_e32 v156, v130, v111
	v_fmac_f32_e32 v157, v131, v111
	v_fmac_f32_e32 v158, v146, v111
	v_fmac_f32_e32 v159, v147, v111
	v_fmac_f32_e32 v182, v132, v112
	v_fmac_f32_e32 v183, v133, v112
	v_fmac_f32_e32 v184, v148, v112
	v_fmac_f32_e32 v185, v149, v112
	v_fmac_f32_e32 v156, v134, v113
	v_fmac_f32_e32 v157, v135, v113
	v_fmac_f32_e32 v158, v150, v113
	v_fmac_f32_e32 v159, v151, v113
	v_fmac_f32_e32 v182, v136, v114
	v_fmac_f32_e32 v183, v137, v114
	v_fmac_f32_e32 v184, v152, v114
	v_fmac_f32_e32 v185, v153, v114
	v_fmac_f32_e32 v156, v138, v115
	v_fmac_f32_e32 v157, v139, v115
	v_fmac_f32_e32 v158, v154, v115
	v_fmac_f32_e32 v159, v155, v115
	v_add_f32_e32 v182, v182, v156
	v_add_f32_e32 v183, v183, v157
	v_add_f32_e32 v184, v184, v158
	v_add_f32_e32 v185, v185, v159
	s_waitcnt vmcnt(31)
	v_cvt_f32_ubyte0_e32 v124, v40
	v_cvt_f32_ubyte1_e32 v126, v40
	v_cvt_f32_ubyte2_e32 v128, v40
	v_cvt_f32_ubyte3_e32 v130, v40
	v_cvt_f32_ubyte0_e32 v132, v41
	v_cvt_f32_ubyte1_e32 v134, v41
	v_cvt_f32_ubyte2_e32 v136, v41
	v_cvt_f32_ubyte3_e32 v138, v41
	s_lshl_b32 s30, s76, 12
	s_add_u32 s28, s26, s30
	s_addc_u32 s29, s27, 0
	global_load_dwordx2 v[40:41], v162, s[28:29]
	v_cvt_f32_ubyte0_e32 v125, v42
	v_cvt_f32_ubyte1_e32 v127, v42
	v_cvt_f32_ubyte2_e32 v129, v42
	v_cvt_f32_ubyte3_e32 v131, v42
	v_cvt_f32_ubyte0_e32 v133, v43
	v_cvt_f32_ubyte1_e32 v135, v43
	v_cvt_f32_ubyte2_e32 v137, v43
	v_cvt_f32_ubyte3_e32 v139, v43
	s_lshl_b32 s30, s77, 12
	s_add_u32 s28, s26, s30
	s_addc_u32 s29, s27, 0
	global_load_dwordx2 v[42:43], v162, s[28:29]
	v_cvt_f32_ubyte0_e32 v140, v44
	v_cvt_f32_ubyte1_e32 v142, v44
	v_cvt_f32_ubyte2_e32 v144, v44
	v_cvt_f32_ubyte3_e32 v146, v44
	v_cvt_f32_ubyte0_e32 v148, v45
	v_cvt_f32_ubyte1_e32 v150, v45
	v_cvt_f32_ubyte2_e32 v152, v45
	v_cvt_f32_ubyte3_e32 v154, v45
	s_lshl_b32 s30, s78, 12
	s_add_u32 s28, s26, s30
	s_addc_u32 s29, s27, 0
	global_load_dwordx2 v[44:45], v162, s[28:29]
	v_cvt_f32_ubyte0_e32 v141, v46
	v_cvt_f32_ubyte1_e32 v143, v46
	v_cvt_f32_ubyte2_e32 v145, v46
	v_cvt_f32_ubyte3_e32 v147, v46
	v_cvt_f32_ubyte0_e32 v149, v47
	v_cvt_f32_ubyte1_e32 v151, v47
	v_cvt_f32_ubyte2_e32 v153, v47
	v_cvt_f32_ubyte3_e32 v155, v47
	s_lshl_b32 s30, s79, 12
	s_add_u32 s28, s26, s30
	s_addc_u32 s29, s27, 0
	global_load_dwordx2 v[46:47], v162, s[28:29]
	v_mul_f32_e32 v186, v124, v108
	v_mul_f32_e32 v187, v125, v108
	v_mul_f32_e32 v188, v140, v108
	v_mul_f32_e32 v189, v141, v108
	v_mul_f32_e32 v156, v126, v109
	v_mul_f32_e32 v157, v127, v109
	v_mul_f32_e32 v158, v142, v109
	v_mul_f32_e32 v159, v143, v109
	v_fmac_f32_e32 v186, v128, v110
	v_fmac_f32_e32 v187, v129, v110
	v_fmac_f32_e32 v188, v144, v110
	v_fmac_f32_e32 v189, v145, v110
	v_fmac_f32_e32 v156, v130, v111
	v_fmac_f32_e32 v157, v131, v111
	v_fmac_f32_e32 v158, v146, v111
	v_fmac_f32_e32 v159, v147, v111
	v_fmac_f32_e32 v186, v132, v112
	v_fmac_f32_e32 v187, v133, v112
	v_fmac_f32_e32 v188, v148, v112
	v_fmac_f32_e32 v189, v149, v112
	v_fmac_f32_e32 v156, v134, v113
	v_fmac_f32_e32 v157, v135, v113
	v_fmac_f32_e32 v158, v150, v113
	v_fmac_f32_e32 v159, v151, v113
	v_fmac_f32_e32 v186, v136, v114
	v_fmac_f32_e32 v187, v137, v114
	v_fmac_f32_e32 v188, v152, v114
	v_fmac_f32_e32 v189, v153, v114
	v_fmac_f32_e32 v156, v138, v115
	v_fmac_f32_e32 v157, v139, v115
	v_fmac_f32_e32 v158, v154, v115
	v_fmac_f32_e32 v159, v155, v115
	v_add_f32_e32 v186, v186, v156
	v_add_f32_e32 v187, v187, v157
	v_add_f32_e32 v188, v188, v158
	v_add_f32_e32 v189, v189, v159
	s_waitcnt vmcnt(31)
	v_cvt_f32_ubyte0_e32 v124, v48
	v_cvt_f32_ubyte1_e32 v126, v48
	v_cvt_f32_ubyte2_e32 v128, v48
	v_cvt_f32_ubyte3_e32 v130, v48
	v_cvt_f32_ubyte0_e32 v132, v49
	v_cvt_f32_ubyte1_e32 v134, v49
	v_cvt_f32_ubyte2_e32 v136, v49
	v_cvt_f32_ubyte3_e32 v138, v49
	s_lshl_b32 s30, s80, 12
	s_add_u32 s28, s26, s30
	s_addc_u32 s29, s27, 0
	global_load_dwordx2 v[48:49], v162, s[28:29]
	v_cvt_f32_ubyte0_e32 v125, v50
	v_cvt_f32_ubyte1_e32 v127, v50
	v_cvt_f32_ubyte2_e32 v129, v50
	v_cvt_f32_ubyte3_e32 v131, v50
	v_cvt_f32_ubyte0_e32 v133, v51
	v_cvt_f32_ubyte1_e32 v135, v51
	v_cvt_f32_ubyte2_e32 v137, v51
	v_cvt_f32_ubyte3_e32 v139, v51
	s_lshl_b32 s30, s81, 12
	s_add_u32 s28, s26, s30
	s_addc_u32 s29, s27, 0
	global_load_dwordx2 v[50:51], v162, s[28:29]
	v_cvt_f32_ubyte0_e32 v140, v52
	v_cvt_f32_ubyte1_e32 v142, v52
	v_cvt_f32_ubyte2_e32 v144, v52
	v_cvt_f32_ubyte3_e32 v146, v52
	v_cvt_f32_ubyte0_e32 v148, v53
	v_cvt_f32_ubyte1_e32 v150, v53
	v_cvt_f32_ubyte2_e32 v152, v53
	v_cvt_f32_ubyte3_e32 v154, v53
	s_lshl_b32 s30, s82, 12
	s_add_u32 s28, s26, s30
	s_addc_u32 s29, s27, 0
	global_load_dwordx2 v[52:53], v162, s[28:29]
	v_cvt_f32_ubyte0_e32 v141, v54
	v_cvt_f32_ubyte1_e32 v143, v54
	v_cvt_f32_ubyte2_e32 v145, v54
	v_cvt_f32_ubyte3_e32 v147, v54
	v_cvt_f32_ubyte0_e32 v149, v55
	v_cvt_f32_ubyte1_e32 v151, v55
	v_cvt_f32_ubyte2_e32 v153, v55
	v_cvt_f32_ubyte3_e32 v155, v55
	s_lshl_b32 s30, s83, 12
	s_add_u32 s28, s26, s30
	s_addc_u32 s29, s27, 0
	global_load_dwordx2 v[54:55], v162, s[28:29]
	v_mul_f32_e32 v190, v124, v108
	v_mul_f32_e32 v191, v125, v108
	v_mul_f32_e32 v192, v140, v108
	v_mul_f32_e32 v193, v141, v108
	v_mul_f32_e32 v156, v126, v109
	v_mul_f32_e32 v157, v127, v109
	v_mul_f32_e32 v158, v142, v109
	v_mul_f32_e32 v159, v143, v109
	v_fmac_f32_e32 v190, v128, v110
	v_fmac_f32_e32 v191, v129, v110
	v_fmac_f32_e32 v192, v144, v110
	v_fmac_f32_e32 v193, v145, v110
	v_fmac_f32_e32 v156, v130, v111
	v_fmac_f32_e32 v157, v131, v111
	v_fmac_f32_e32 v158, v146, v111
	v_fmac_f32_e32 v159, v147, v111
	v_fmac_f32_e32 v190, v132, v112
	v_fmac_f32_e32 v191, v133, v112
	v_fmac_f32_e32 v192, v148, v112
	v_fmac_f32_e32 v193, v149, v112
	v_fmac_f32_e32 v156, v134, v113
	v_fmac_f32_e32 v157, v135, v113
	v_fmac_f32_e32 v158, v150, v113
	v_fmac_f32_e32 v159, v151, v113
	v_fmac_f32_e32 v190, v136, v114
	v_fmac_f32_e32 v191, v137, v114
	v_fmac_f32_e32 v192, v152, v114
	v_fmac_f32_e32 v193, v153, v114
	v_fmac_f32_e32 v156, v138, v115
	v_fmac_f32_e32 v157, v139, v115
	v_fmac_f32_e32 v158, v154, v115
	v_fmac_f32_e32 v159, v155, v115
	v_add_f32_e32 v190, v190, v156
	v_add_f32_e32 v191, v191, v157
	v_add_f32_e32 v192, v192, v158
	v_add_f32_e32 v193, v193, v159
	s_waitcnt vmcnt(31)
	v_cvt_f32_ubyte0_e32 v124, v56
	v_cvt_f32_ubyte1_e32 v126, v56
	v_cvt_f32_ubyte2_e32 v128, v56
	v_cvt_f32_ubyte3_e32 v130, v56
	v_cvt_f32_ubyte0_e32 v132, v57
	v_cvt_f32_ubyte1_e32 v134, v57
	v_cvt_f32_ubyte2_e32 v136, v57
	v_cvt_f32_ubyte3_e32 v138, v57
	s_waitcnt lgkmcnt(0)
	s_load_dwordx16 s[68:83], s[36:37], 0x100 glc
	s_lshl_b32 s30, s84, 12
	s_add_u32 s28, s26, s30
	s_addc_u32 s29, s27, 0
	global_load_dwordx2 v[56:57], v162, s[28:29]
	v_cvt_f32_ubyte0_e32 v125, v58
	v_cvt_f32_ubyte1_e32 v127, v58
	v_cvt_f32_ubyte2_e32 v129, v58
	v_cvt_f32_ubyte3_e32 v131, v58
	v_cvt_f32_ubyte0_e32 v133, v59
	v_cvt_f32_ubyte1_e32 v135, v59
	v_cvt_f32_ubyte2_e32 v137, v59
	v_cvt_f32_ubyte3_e32 v139, v59
	s_lshl_b32 s30, s85, 12
	s_add_u32 s28, s26, s30
	s_addc_u32 s29, s27, 0
	global_load_dwordx2 v[58:59], v162, s[28:29]
	v_cvt_f32_ubyte0_e32 v140, v60
	v_cvt_f32_ubyte1_e32 v142, v60
	v_cvt_f32_ubyte2_e32 v144, v60
	v_cvt_f32_ubyte3_e32 v146, v60
	v_cvt_f32_ubyte0_e32 v148, v61
	v_cvt_f32_ubyte1_e32 v150, v61
	v_cvt_f32_ubyte2_e32 v152, v61
	v_cvt_f32_ubyte3_e32 v154, v61
	s_lshl_b32 s30, s86, 12
	s_add_u32 s28, s26, s30
	s_addc_u32 s29, s27, 0
	global_load_dwordx2 v[60:61], v162, s[28:29]
	v_cvt_f32_ubyte0_e32 v141, v62
	v_cvt_f32_ubyte1_e32 v143, v62
	v_cvt_f32_ubyte2_e32 v145, v62
	v_cvt_f32_ubyte3_e32 v147, v62
	v_cvt_f32_ubyte0_e32 v149, v63
	v_cvt_f32_ubyte1_e32 v151, v63
	v_cvt_f32_ubyte2_e32 v153, v63
	v_cvt_f32_ubyte3_e32 v155, v63
	s_lshl_b32 s30, s87, 12
	s_add_u32 s28, s26, s30
	s_addc_u32 s29, s27, 0
	global_load_dwordx2 v[62:63], v162, s[28:29]
	v_mul_f32_e32 v194, v124, v108
	v_mul_f32_e32 v195, v125, v108
	v_mul_f32_e32 v196, v140, v108
	v_mul_f32_e32 v197, v141, v108
	v_mul_f32_e32 v156, v126, v109
	v_mul_f32_e32 v157, v127, v109
	v_mul_f32_e32 v158, v142, v109
	v_mul_f32_e32 v159, v143, v109
	v_fmac_f32_e32 v194, v128, v110
	v_fmac_f32_e32 v195, v129, v110
	v_fmac_f32_e32 v196, v144, v110
	v_fmac_f32_e32 v197, v145, v110
	v_fmac_f32_e32 v156, v130, v111
	v_fmac_f32_e32 v157, v131, v111
	v_fmac_f32_e32 v158, v146, v111
	v_fmac_f32_e32 v159, v147, v111
	v_fmac_f32_e32 v194, v132, v112
	v_fmac_f32_e32 v195, v133, v112
	v_fmac_f32_e32 v196, v148, v112
	v_fmac_f32_e32 v197, v149, v112
	v_fmac_f32_e32 v156, v134, v113
	v_fmac_f32_e32 v157, v135, v113
	v_fmac_f32_e32 v158, v150, v113
	v_fmac_f32_e32 v159, v151, v113
	v_fmac_f32_e32 v194, v136, v114
	v_fmac_f32_e32 v195, v137, v114
	v_fmac_f32_e32 v196, v152, v114
	v_fmac_f32_e32 v197, v153, v114
	v_fmac_f32_e32 v156, v138, v115
	v_fmac_f32_e32 v157, v139, v115
	v_fmac_f32_e32 v158, v154, v115
	v_fmac_f32_e32 v159, v155, v115
	v_add_f32_e32 v194, v194, v156
	v_add_f32_e32 v195, v195, v157
	v_add_f32_e32 v196, v196, v158
	v_add_f32_e32 v197, v197, v159
	s_waitcnt vmcnt(31)
	v_cvt_f32_ubyte0_e32 v124, v64
	v_cvt_f32_ubyte1_e32 v126, v64
	v_cvt_f32_ubyte2_e32 v128, v64
	v_cvt_f32_ubyte3_e32 v130, v64
	v_cvt_f32_ubyte0_e32 v132, v65
	v_cvt_f32_ubyte1_e32 v134, v65
	v_cvt_f32_ubyte2_e32 v136, v65
	v_cvt_f32_ubyte3_e32 v138, v65
	s_lshl_b32 s30, s88, 12
	s_add_u32 s28, s26, s30
	s_addc_u32 s29, s27, 0
	global_load_dwordx2 v[64:65], v162, s[28:29]
	v_cvt_f32_ubyte0_e32 v125, v66
	v_cvt_f32_ubyte1_e32 v127, v66
	v_cvt_f32_ubyte2_e32 v129, v66
	v_cvt_f32_ubyte3_e32 v131, v66
	v_cvt_f32_ubyte0_e32 v133, v67
	v_cvt_f32_ubyte1_e32 v135, v67
	v_cvt_f32_ubyte2_e32 v137, v67
	v_cvt_f32_ubyte3_e32 v139, v67
	s_lshl_b32 s30, s89, 12
	s_add_u32 s28, s26, s30
	s_addc_u32 s29, s27, 0
	global_load_dwordx2 v[66:67], v162, s[28:29]
	v_cvt_f32_ubyte0_e32 v140, v68
	v_cvt_f32_ubyte1_e32 v142, v68
	v_cvt_f32_ubyte2_e32 v144, v68
	v_cvt_f32_ubyte3_e32 v146, v68
	v_cvt_f32_ubyte0_e32 v148, v69
	v_cvt_f32_ubyte1_e32 v150, v69
	v_cvt_f32_ubyte2_e32 v152, v69
	v_cvt_f32_ubyte3_e32 v154, v69
	s_lshl_b32 s30, s90, 12
	s_add_u32 s28, s26, s30
	s_addc_u32 s29, s27, 0
	global_load_dwordx2 v[68:69], v162, s[28:29]
	v_cvt_f32_ubyte0_e32 v141, v70
	v_cvt_f32_ubyte1_e32 v143, v70
	v_cvt_f32_ubyte2_e32 v145, v70
	v_cvt_f32_ubyte3_e32 v147, v70
	v_cvt_f32_ubyte0_e32 v149, v71
	v_cvt_f32_ubyte1_e32 v151, v71
	v_cvt_f32_ubyte2_e32 v153, v71
	v_cvt_f32_ubyte3_e32 v155, v71
	s_lshl_b32 s30, s91, 12
	s_add_u32 s28, s26, s30
	s_addc_u32 s29, s27, 0
	global_load_dwordx2 v[70:71], v162, s[28:29]
	v_mul_f32_e32 v198, v124, v108
	v_mul_f32_e32 v199, v125, v108
	v_mul_f32_e32 v200, v140, v108
	v_mul_f32_e32 v201, v141, v108
	v_mul_f32_e32 v156, v126, v109
	v_mul_f32_e32 v157, v127, v109
	v_mul_f32_e32 v158, v142, v109
	v_mul_f32_e32 v159, v143, v109
	v_fmac_f32_e32 v198, v128, v110
	v_fmac_f32_e32 v199, v129, v110
	v_fmac_f32_e32 v200, v144, v110
	v_fmac_f32_e32 v201, v145, v110
	v_fmac_f32_e32 v156, v130, v111
	v_fmac_f32_e32 v157, v131, v111
	v_fmac_f32_e32 v158, v146, v111
	v_fmac_f32_e32 v159, v147, v111
	v_fmac_f32_e32 v198, v132, v112
	v_fmac_f32_e32 v199, v133, v112
	v_fmac_f32_e32 v200, v148, v112
	v_fmac_f32_e32 v201, v149, v112
	v_fmac_f32_e32 v156, v134, v113
	v_fmac_f32_e32 v157, v135, v113
	v_fmac_f32_e32 v158, v150, v113
	v_fmac_f32_e32 v159, v151, v113
	v_fmac_f32_e32 v198, v136, v114
	v_fmac_f32_e32 v199, v137, v114
	v_fmac_f32_e32 v200, v152, v114
	v_fmac_f32_e32 v201, v153, v114
	v_fmac_f32_e32 v156, v138, v115
	v_fmac_f32_e32 v157, v139, v115
	v_fmac_f32_e32 v158, v154, v115
	v_fmac_f32_e32 v159, v155, v115
	v_add_f32_e32 v198, v198, v156
	v_add_f32_e32 v199, v199, v157
	v_add_f32_e32 v200, v200, v158
	v_add_f32_e32 v201, v201, v159
	s_waitcnt vmcnt(31)
	v_cvt_f32_ubyte0_e32 v124, v72
	v_cvt_f32_ubyte1_e32 v126, v72
	v_cvt_f32_ubyte2_e32 v128, v72
	v_cvt_f32_ubyte3_e32 v130, v72
	v_cvt_f32_ubyte0_e32 v132, v73
	v_cvt_f32_ubyte1_e32 v134, v73
	v_cvt_f32_ubyte2_e32 v136, v73
	v_cvt_f32_ubyte3_e32 v138, v73
	s_lshl_b32 s30, s92, 12
	s_add_u32 s28, s26, s30
	s_addc_u32 s29, s27, 0
	global_load_dwordx2 v[72:73], v162, s[28:29]
	v_cvt_f32_ubyte0_e32 v125, v74
	v_cvt_f32_ubyte1_e32 v127, v74
	v_cvt_f32_ubyte2_e32 v129, v74
	v_cvt_f32_ubyte3_e32 v131, v74
	v_cvt_f32_ubyte0_e32 v133, v75
	v_cvt_f32_ubyte1_e32 v135, v75
	v_cvt_f32_ubyte2_e32 v137, v75
	v_cvt_f32_ubyte3_e32 v139, v75
	s_lshl_b32 s30, s93, 12
	s_add_u32 s28, s26, s30
	s_addc_u32 s29, s27, 0
	global_load_dwordx2 v[74:75], v162, s[28:29]
	v_cvt_f32_ubyte0_e32 v140, v76
	v_cvt_f32_ubyte1_e32 v142, v76
	v_cvt_f32_ubyte2_e32 v144, v76
	v_cvt_f32_ubyte3_e32 v146, v76
	v_cvt_f32_ubyte0_e32 v148, v77
	v_cvt_f32_ubyte1_e32 v150, v77
	v_cvt_f32_ubyte2_e32 v152, v77
	v_cvt_f32_ubyte3_e32 v154, v77
	s_lshl_b32 s30, s94, 12
	s_add_u32 s28, s26, s30
	s_addc_u32 s29, s27, 0
	global_load_dwordx2 v[76:77], v162, s[28:29]
	v_cvt_f32_ubyte0_e32 v141, v78
	v_cvt_f32_ubyte1_e32 v143, v78
	v_cvt_f32_ubyte2_e32 v145, v78
	v_cvt_f32_ubyte3_e32 v147, v78
	v_cvt_f32_ubyte0_e32 v149, v79
	v_cvt_f32_ubyte1_e32 v151, v79
	v_cvt_f32_ubyte2_e32 v153, v79
	v_cvt_f32_ubyte3_e32 v155, v79
	s_lshl_b32 s30, s95, 12
	s_add_u32 s28, s26, s30
	s_addc_u32 s29, s27, 0
	global_load_dwordx2 v[78:79], v162, s[28:29]
	v_mul_f32_e32 v202, v124, v108
	v_mul_f32_e32 v203, v125, v108
	v_mul_f32_e32 v204, v140, v108
	v_mul_f32_e32 v205, v141, v108
	v_mul_f32_e32 v156, v126, v109
	v_mul_f32_e32 v157, v127, v109
	v_mul_f32_e32 v158, v142, v109
	v_mul_f32_e32 v159, v143, v109
	v_fmac_f32_e32 v202, v128, v110
	v_fmac_f32_e32 v203, v129, v110
	v_fmac_f32_e32 v204, v144, v110
	v_fmac_f32_e32 v205, v145, v110
	v_fmac_f32_e32 v156, v130, v111
	v_fmac_f32_e32 v157, v131, v111
	v_fmac_f32_e32 v158, v146, v111
	v_fmac_f32_e32 v159, v147, v111
	v_fmac_f32_e32 v202, v132, v112
	v_fmac_f32_e32 v203, v133, v112
	v_fmac_f32_e32 v204, v148, v112
	v_fmac_f32_e32 v205, v149, v112
	v_fmac_f32_e32 v156, v134, v113
	v_fmac_f32_e32 v157, v135, v113
	v_fmac_f32_e32 v158, v150, v113
	v_fmac_f32_e32 v159, v151, v113
	v_fmac_f32_e32 v202, v136, v114
	v_fmac_f32_e32 v203, v137, v114
	v_fmac_f32_e32 v204, v152, v114
	v_fmac_f32_e32 v205, v153, v114
	v_fmac_f32_e32 v156, v138, v115
	v_fmac_f32_e32 v157, v139, v115
	v_fmac_f32_e32 v158, v154, v115
	v_fmac_f32_e32 v159, v155, v115
	v_add_f32_e32 v202, v202, v156
	v_add_f32_e32 v203, v203, v157
	v_add_f32_e32 v204, v204, v158
	v_add_f32_e32 v205, v205, v159
	s_waitcnt vmcnt(31)
	v_cvt_f32_ubyte0_e32 v124, v80
	v_cvt_f32_ubyte1_e32 v126, v80
	v_cvt_f32_ubyte2_e32 v128, v80
	v_cvt_f32_ubyte3_e32 v130, v80
	v_cvt_f32_ubyte0_e32 v132, v81
	v_cvt_f32_ubyte1_e32 v134, v81
	v_cvt_f32_ubyte2_e32 v136, v81
	v_cvt_f32_ubyte3_e32 v138, v81
	s_lshl_b32 s30, s96, 12
	s_add_u32 s28, s26, s30
	s_addc_u32 s29, s27, 0
	global_load_dwordx2 v[80:81], v162, s[28:29]
	v_cvt_f32_ubyte0_e32 v125, v82
	v_cvt_f32_ubyte1_e32 v127, v82
	v_cvt_f32_ubyte2_e32 v129, v82
	v_cvt_f32_ubyte3_e32 v131, v82
	v_cvt_f32_ubyte0_e32 v133, v83
	v_cvt_f32_ubyte1_e32 v135, v83
	v_cvt_f32_ubyte2_e32 v137, v83
	v_cvt_f32_ubyte3_e32 v139, v83
	s_lshl_b32 s30, s97, 12
	s_add_u32 s28, s26, s30
	s_addc_u32 s29, s27, 0
	global_load_dwordx2 v[82:83], v162, s[28:29]
	v_cvt_f32_ubyte0_e32 v140, v84
	v_cvt_f32_ubyte1_e32 v142, v84
	v_cvt_f32_ubyte2_e32 v144, v84
	v_cvt_f32_ubyte3_e32 v146, v84
	v_cvt_f32_ubyte0_e32 v148, v85
	v_cvt_f32_ubyte1_e32 v150, v85
	v_cvt_f32_ubyte2_e32 v152, v85
	v_cvt_f32_ubyte3_e32 v154, v85
	s_lshl_b32 s30, s98, 12
	s_add_u32 s28, s26, s30
	s_addc_u32 s29, s27, 0
	global_load_dwordx2 v[84:85], v162, s[28:29]
	v_cvt_f32_ubyte0_e32 v141, v86
	v_cvt_f32_ubyte1_e32 v143, v86
	v_cvt_f32_ubyte2_e32 v145, v86
	v_cvt_f32_ubyte3_e32 v147, v86
	v_cvt_f32_ubyte0_e32 v149, v87
	v_cvt_f32_ubyte1_e32 v151, v87
	v_cvt_f32_ubyte2_e32 v153, v87
	v_cvt_f32_ubyte3_e32 v155, v87
	s_lshl_b32 s30, s99, 12
	s_add_u32 s28, s26, s30
	s_addc_u32 s29, s27, 0
	global_load_dwordx2 v[86:87], v162, s[28:29]
	v_mul_f32_e32 v206, v124, v108
	v_mul_f32_e32 v207, v125, v108
	v_mul_f32_e32 v208, v140, v108
	v_mul_f32_e32 v209, v141, v108
	v_mul_f32_e32 v156, v126, v109
	v_mul_f32_e32 v157, v127, v109
	v_mul_f32_e32 v158, v142, v109
	v_mul_f32_e32 v159, v143, v109
	v_fmac_f32_e32 v206, v128, v110
	v_fmac_f32_e32 v207, v129, v110
	v_fmac_f32_e32 v208, v144, v110
	v_fmac_f32_e32 v209, v145, v110
	v_fmac_f32_e32 v156, v130, v111
	v_fmac_f32_e32 v157, v131, v111
	v_fmac_f32_e32 v158, v146, v111
	v_fmac_f32_e32 v159, v147, v111
	v_fmac_f32_e32 v206, v132, v112
	v_fmac_f32_e32 v207, v133, v112
	v_fmac_f32_e32 v208, v148, v112
	v_fmac_f32_e32 v209, v149, v112
	v_fmac_f32_e32 v156, v134, v113
	v_fmac_f32_e32 v157, v135, v113
	v_fmac_f32_e32 v158, v150, v113
	v_fmac_f32_e32 v159, v151, v113
	v_fmac_f32_e32 v206, v136, v114
	v_fmac_f32_e32 v207, v137, v114
	v_fmac_f32_e32 v208, v152, v114
	v_fmac_f32_e32 v209, v153, v114
	v_fmac_f32_e32 v156, v138, v115
	v_fmac_f32_e32 v157, v139, v115
	v_fmac_f32_e32 v158, v154, v115
	v_fmac_f32_e32 v159, v155, v115
	v_add_f32_e32 v206, v206, v156
	v_add_f32_e32 v207, v207, v157
	v_add_f32_e32 v208, v208, v158
	v_add_f32_e32 v209, v209, v159
	v_permlane32_swap_b32_e32 v178, v194
	v_permlane32_swap_b32_e32 v179, v195
	v_permlane32_swap_b32_e32 v180, v196
	v_permlane32_swap_b32_e32 v181, v197
	v_permlane32_swap_b32_e32 v182, v198
	v_permlane32_swap_b32_e32 v183, v199
	v_permlane32_swap_b32_e32 v184, v200
	v_permlane32_swap_b32_e32 v185, v201
	v_permlane32_swap_b32_e32 v186, v202
	v_permlane32_swap_b32_e32 v187, v203
	v_permlane32_swap_b32_e32 v188, v204
	v_permlane32_swap_b32_e32 v189, v205
	v_permlane32_swap_b32_e32 v190, v206
	v_permlane32_swap_b32_e32 v191, v207
	v_permlane32_swap_b32_e32 v192, v208
	v_permlane32_swap_b32_e32 v193, v209
	v_add_f32_e32 v178, v178, v194
	v_add_f32_e32 v179, v179, v195
	v_add_f32_e32 v180, v180, v196
	v_add_f32_e32 v181, v181, v197
	v_add_f32_e32 v182, v182, v198
	v_add_f32_e32 v183, v183, v199
	v_add_f32_e32 v184, v184, v200
	v_add_f32_e32 v185, v185, v201
	v_add_f32_e32 v186, v186, v202
	v_add_f32_e32 v187, v187, v203
	v_add_f32_e32 v188, v188, v204
	v_add_f32_e32 v189, v189, v205
	v_add_f32_e32 v190, v190, v206
	v_add_f32_e32 v191, v191, v207
	v_add_f32_e32 v192, v192, v208
	v_add_f32_e32 v193, v193, v209
	v_permlane16_swap_b32_e32 v178, v186
	v_permlane16_swap_b32_e32 v179, v187
	v_permlane16_swap_b32_e32 v180, v188
	v_permlane16_swap_b32_e32 v181, v189
	v_permlane16_swap_b32_e32 v182, v190
	v_permlane16_swap_b32_e32 v183, v191
	v_permlane16_swap_b32_e32 v184, v192
	v_permlane16_swap_b32_e32 v185, v193
	v_add_f32_e32 v178, v178, v186
	v_add_f32_e32 v179, v179, v187
	v_add_f32_e32 v180, v180, v188
	v_add_f32_e32 v181, v181, v189
	v_add_f32_e32 v182, v182, v190
	v_add_f32_e32 v183, v183, v191
	v_add_f32_e32 v184, v184, v192
	v_add_f32_e32 v185, v185, v193
	v_cndmask_b32_e64 v2, v178, v182, s[8:9]
	v_cndmask_b32_e64 v3, v179, v183, s[8:9]
	v_cndmask_b32_e64 v4, v180, v184, s[8:9]
	v_cndmask_b32_e64 v5, v181, v185, s[8:9]
	v_cndmask_b32_e64 v6, v182, v178, s[8:9]
	v_cndmask_b32_e64 v7, v183, v179, s[8:9]
	v_cndmask_b32_e64 v8, v184, v180, s[8:9]
	v_cndmask_b32_e64 v9, v185, v181, s[8:9]
	v_add_f32_dpp v6, v2, v6 row_ror:8 row_mask:0xf bank_mask:0xf
	v_add_f32_dpp v7, v3, v7 row_ror:8 row_mask:0xf bank_mask:0xf
	v_add_f32_dpp v8, v4, v8 row_ror:8 row_mask:0xf bank_mask:0xf
	v_add_f32_dpp v9, v5, v9 row_ror:8 row_mask:0xf bank_mask:0xf
	v_cndmask_b32_e64 v2, v6, v8, s[10:11]
	v_cndmask_b32_e64 v3, v7, v9, s[10:11]
	v_cndmask_b32_e64 v4, v8, v6, s[10:11]
	v_cndmask_b32_e64 v5, v9, v7, s[10:11]
	v_add_f32_dpp v4, v2, v4 row_half_mirror row_mask:0xf bank_mask:0xf
	v_add_f32_dpp v5, v3, v5 row_half_mirror row_mask:0xf bank_mask:0xf
	v_cndmask_b32_e64 v2, v4, v5, s[14:15]
	v_cndmask_b32_e64 v3, v5, v4, s[14:15]
	s_nop 0
	v_add_f32_dpp v3, v2, v3 quad_perm:[2,3,0,1] row_mask:0xf bank_mask:0xf
	s_nop 1
	v_add_f32_dpp v11, v3, v3 quad_perm:[1,0,3,2] row_mask:0xf bank_mask:0xf
	s_mov_b64 exec, s[2:3]
	global_store_dword v[22:23], v11, off
	s_mov_b64 exec, -1
	s_waitcnt vmcnt(29)
	v_cvt_f32_ubyte0_e32 v124, v24
	v_cvt_f32_ubyte1_e32 v126, v24
	v_cvt_f32_ubyte2_e32 v128, v24
	v_cvt_f32_ubyte3_e32 v130, v24
	v_cvt_f32_ubyte0_e32 v132, v25
	v_cvt_f32_ubyte1_e32 v134, v25
	v_cvt_f32_ubyte2_e32 v136, v25
	v_cvt_f32_ubyte3_e32 v138, v25
	s_waitcnt lgkmcnt(0)
	s_load_dwordx16 s[84:99], s[36:37], 0x140 glc
	s_lshl_b32 s30, s68, 12
	s_add_u32 s28, s26, s30
	s_addc_u32 s29, s27, 0
	global_load_dwordx2 v[24:25], v162, s[28:29]
	v_cvt_f32_ubyte0_e32 v125, v26
	v_cvt_f32_ubyte1_e32 v127, v26
	v_cvt_f32_ubyte2_e32 v129, v26
	v_cvt_f32_ubyte3_e32 v131, v26
	v_cvt_f32_ubyte0_e32 v133, v27
	v_cvt_f32_ubyte1_e32 v135, v27
	v_cvt_f32_ubyte2_e32 v137, v27
	v_cvt_f32_ubyte3_e32 v139, v27
	s_lshl_b32 s30, s69, 12
	s_add_u32 s28, s26, s30
	s_addc_u32 s29, s27, 0
	global_load_dwordx2 v[26:27], v162, s[28:29]
	v_cvt_f32_ubyte0_e32 v140, v28
	v_cvt_f32_ubyte1_e32 v142, v28
	v_cvt_f32_ubyte2_e32 v144, v28
	v_cvt_f32_ubyte3_e32 v146, v28
	v_cvt_f32_ubyte0_e32 v148, v29
	v_cvt_f32_ubyte1_e32 v150, v29
	v_cvt_f32_ubyte2_e32 v152, v29
	v_cvt_f32_ubyte3_e32 v154, v29
	s_lshl_b32 s30, s70, 12
	s_add_u32 s28, s26, s30
	s_addc_u32 s29, s27, 0
	global_load_dwordx2 v[28:29], v162, s[28:29]
	v_cvt_f32_ubyte0_e32 v141, v30
	v_cvt_f32_ubyte1_e32 v143, v30
	v_cvt_f32_ubyte2_e32 v145, v30
	v_cvt_f32_ubyte3_e32 v147, v30
	v_cvt_f32_ubyte0_e32 v149, v31
	v_cvt_f32_ubyte1_e32 v151, v31
	v_cvt_f32_ubyte2_e32 v153, v31
	v_cvt_f32_ubyte3_e32 v155, v31
	s_lshl_b32 s30, s71, 12
	s_add_u32 s28, s26, s30
	s_addc_u32 s29, s27, 0
	global_load_dwordx2 v[30:31], v162, s[28:29]
	v_mul_f32_e32 v178, v124, v108
	v_mul_f32_e32 v179, v125, v108
	v_mul_f32_e32 v180, v140, v108
	v_mul_f32_e32 v181, v141, v108
	v_mul_f32_e32 v156, v126, v109
	v_mul_f32_e32 v157, v127, v109
	v_mul_f32_e32 v158, v142, v109
	v_mul_f32_e32 v159, v143, v109
	v_fmac_f32_e32 v178, v128, v110
	v_fmac_f32_e32 v179, v129, v110
	v_fmac_f32_e32 v180, v144, v110
	v_fmac_f32_e32 v181, v145, v110
	v_fmac_f32_e32 v156, v130, v111
	v_fmac_f32_e32 v157, v131, v111
	v_fmac_f32_e32 v158, v146, v111
	v_fmac_f32_e32 v159, v147, v111
	v_fmac_f32_e32 v178, v132, v112
	v_fmac_f32_e32 v179, v133, v112
	v_fmac_f32_e32 v180, v148, v112
	v_fmac_f32_e32 v181, v149, v112
	v_fmac_f32_e32 v156, v134, v113
	v_fmac_f32_e32 v157, v135, v113
	v_fmac_f32_e32 v158, v150, v113
	v_fmac_f32_e32 v159, v151, v113
	v_fmac_f32_e32 v178, v136, v114
	v_fmac_f32_e32 v179, v137, v114
	v_fmac_f32_e32 v180, v152, v114
	v_fmac_f32_e32 v181, v153, v114
	v_fmac_f32_e32 v156, v138, v115
	v_fmac_f32_e32 v157, v139, v115
	v_fmac_f32_e32 v158, v154, v115
	v_fmac_f32_e32 v159, v155, v115
	v_add_f32_e32 v178, v178, v156
	v_add_f32_e32 v179, v179, v157
	v_add_f32_e32 v180, v180, v158
	v_add_f32_e32 v181, v181, v159
	s_waitcnt vmcnt(29)
	v_cvt_f32_ubyte0_e32 v124, v32
	v_cvt_f32_ubyte1_e32 v126, v32
	v_cvt_f32_ubyte2_e32 v128, v32
	v_cvt_f32_ubyte3_e32 v130, v32
	v_cvt_f32_ubyte0_e32 v132, v33
	v_cvt_f32_ubyte1_e32 v134, v33
	v_cvt_f32_ubyte2_e32 v136, v33
	v_cvt_f32_ubyte3_e32 v138, v33
	s_lshl_b32 s30, s72, 12
	s_add_u32 s28, s26, s30
	s_addc_u32 s29, s27, 0
	global_load_dwordx2 v[32:33], v162, s[28:29]
	v_cvt_f32_ubyte0_e32 v125, v34
	v_cvt_f32_ubyte1_e32 v127, v34
	v_cvt_f32_ubyte2_e32 v129, v34
	v_cvt_f32_ubyte3_e32 v131, v34
	v_cvt_f32_ubyte0_e32 v133, v35
	v_cvt_f32_ubyte1_e32 v135, v35
	v_cvt_f32_ubyte2_e32 v137, v35
	v_cvt_f32_ubyte3_e32 v139, v35
	s_lshl_b32 s30, s73, 12
	s_add_u32 s28, s26, s30
	s_addc_u32 s29, s27, 0
	global_load_dwordx2 v[34:35], v162, s[28:29]
	v_cvt_f32_ubyte0_e32 v140, v36
	v_cvt_f32_ubyte1_e32 v142, v36
	v_cvt_f32_ubyte2_e32 v144, v36
	v_cvt_f32_ubyte3_e32 v146, v36
	v_cvt_f32_ubyte0_e32 v148, v37
	v_cvt_f32_ubyte1_e32 v150, v37
	v_cvt_f32_ubyte2_e32 v152, v37
	v_cvt_f32_ubyte3_e32 v154, v37
	s_lshl_b32 s30, s74, 12
	s_add_u32 s28, s26, s30
	s_addc_u32 s29, s27, 0
	global_load_dwordx2 v[36:37], v162, s[28:29]
	v_cvt_f32_ubyte0_e32 v141, v38
	v_cvt_f32_ubyte1_e32 v143, v38
	v_cvt_f32_ubyte2_e32 v145, v38
	v_cvt_f32_ubyte3_e32 v147, v38
	v_cvt_f32_ubyte0_e32 v149, v39
	v_cvt_f32_ubyte1_e32 v151, v39
	v_cvt_f32_ubyte2_e32 v153, v39
	v_cvt_f32_ubyte3_e32 v155, v39
	s_lshl_b32 s30, s75, 12
	s_add_u32 s28, s26, s30
	s_addc_u32 s29, s27, 0
	global_load_dwordx2 v[38:39], v162, s[28:29]
	v_mul_f32_e32 v182, v124, v108
	v_mul_f32_e32 v183, v125, v108
	v_mul_f32_e32 v184, v140, v108
	v_mul_f32_e32 v185, v141, v108
	v_mul_f32_e32 v156, v126, v109
	v_mul_f32_e32 v157, v127, v109
	v_mul_f32_e32 v158, v142, v109
	v_mul_f32_e32 v159, v143, v109
	v_fmac_f32_e32 v182, v128, v110
	v_fmac_f32_e32 v183, v129, v110
	v_fmac_f32_e32 v184, v144, v110
	v_fmac_f32_e32 v185, v145, v110
	v_fmac_f32_e32 v156, v130, v111
	v_fmac_f32_e32 v157, v131, v111
	v_fmac_f32_e32 v158, v146, v111
	v_fmac_f32_e32 v159, v147, v111
	v_fmac_f32_e32 v182, v132, v112
	v_fmac_f32_e32 v183, v133, v112
	v_fmac_f32_e32 v184, v148, v112
	v_fmac_f32_e32 v185, v149, v112
	v_fmac_f32_e32 v156, v134, v113
	v_fmac_f32_e32 v157, v135, v113
	v_fmac_f32_e32 v158, v150, v113
	v_fmac_f32_e32 v159, v151, v113
	v_fmac_f32_e32 v182, v136, v114
	v_fmac_f32_e32 v183, v137, v114
	v_fmac_f32_e32 v184, v152, v114
	v_fmac_f32_e32 v185, v153, v114
	v_fmac_f32_e32 v156, v138, v115
	v_fmac_f32_e32 v157, v139, v115
	v_fmac_f32_e32 v158, v154, v115
	v_fmac_f32_e32 v159, v155, v115
	v_add_f32_e32 v182, v182, v156
	v_add_f32_e32 v183, v183, v157
	v_add_f32_e32 v184, v184, v158
	v_add_f32_e32 v185, v185, v159
	s_waitcnt vmcnt(29)
	v_cvt_f32_ubyte0_e32 v124, v40
	v_cvt_f32_ubyte1_e32 v126, v40
	v_cvt_f32_ubyte2_e32 v128, v40
	v_cvt_f32_ubyte3_e32 v130, v40
	v_cvt_f32_ubyte0_e32 v132, v41
	v_cvt_f32_ubyte1_e32 v134, v41
	v_cvt_f32_ubyte2_e32 v136, v41
	v_cvt_f32_ubyte3_e32 v138, v41
	s_lshl_b32 s30, s76, 12
	s_add_u32 s28, s26, s30
	s_addc_u32 s29, s27, 0
	global_load_dwordx2 v[40:41], v162, s[28:29]
	v_cvt_f32_ubyte0_e32 v125, v42
	v_cvt_f32_ubyte1_e32 v127, v42
	v_cvt_f32_ubyte2_e32 v129, v42
	v_cvt_f32_ubyte3_e32 v131, v42
	v_cvt_f32_ubyte0_e32 v133, v43
	v_cvt_f32_ubyte1_e32 v135, v43
	v_cvt_f32_ubyte2_e32 v137, v43
	v_cvt_f32_ubyte3_e32 v139, v43
	s_lshl_b32 s30, s77, 12
	s_add_u32 s28, s26, s30
	s_addc_u32 s29, s27, 0
	global_load_dwordx2 v[42:43], v162, s[28:29]
	v_cvt_f32_ubyte0_e32 v140, v44
	v_cvt_f32_ubyte1_e32 v142, v44
	v_cvt_f32_ubyte2_e32 v144, v44
	v_cvt_f32_ubyte3_e32 v146, v44
	v_cvt_f32_ubyte0_e32 v148, v45
	v_cvt_f32_ubyte1_e32 v150, v45
	v_cvt_f32_ubyte2_e32 v152, v45
	v_cvt_f32_ubyte3_e32 v154, v45
	s_lshl_b32 s30, s78, 12
	s_add_u32 s28, s26, s30
	s_addc_u32 s29, s27, 0
	global_load_dwordx2 v[44:45], v162, s[28:29]
	v_cvt_f32_ubyte0_e32 v141, v46
	v_cvt_f32_ubyte1_e32 v143, v46
	v_cvt_f32_ubyte2_e32 v145, v46
	v_cvt_f32_ubyte3_e32 v147, v46
	v_cvt_f32_ubyte0_e32 v149, v47
	v_cvt_f32_ubyte1_e32 v151, v47
	v_cvt_f32_ubyte2_e32 v153, v47
	v_cvt_f32_ubyte3_e32 v155, v47
	s_lshl_b32 s30, s79, 12
	s_add_u32 s28, s26, s30
	s_addc_u32 s29, s27, 0
	global_load_dwordx2 v[46:47], v162, s[28:29]
	v_mul_f32_e32 v186, v124, v108
	v_mul_f32_e32 v187, v125, v108
	v_mul_f32_e32 v188, v140, v108
	v_mul_f32_e32 v189, v141, v108
	v_mul_f32_e32 v156, v126, v109
	v_mul_f32_e32 v157, v127, v109
	v_mul_f32_e32 v158, v142, v109
	v_mul_f32_e32 v159, v143, v109
	v_fmac_f32_e32 v186, v128, v110
	v_fmac_f32_e32 v187, v129, v110
	v_fmac_f32_e32 v188, v144, v110
	v_fmac_f32_e32 v189, v145, v110
	v_fmac_f32_e32 v156, v130, v111
	v_fmac_f32_e32 v157, v131, v111
	v_fmac_f32_e32 v158, v146, v111
	v_fmac_f32_e32 v159, v147, v111
	v_fmac_f32_e32 v186, v132, v112
	v_fmac_f32_e32 v187, v133, v112
	v_fmac_f32_e32 v188, v148, v112
	v_fmac_f32_e32 v189, v149, v112
	v_fmac_f32_e32 v156, v134, v113
	v_fmac_f32_e32 v157, v135, v113
	v_fmac_f32_e32 v158, v150, v113
	v_fmac_f32_e32 v159, v151, v113
	v_fmac_f32_e32 v186, v136, v114
	v_fmac_f32_e32 v187, v137, v114
	v_fmac_f32_e32 v188, v152, v114
	v_fmac_f32_e32 v189, v153, v114
	v_fmac_f32_e32 v156, v138, v115
	v_fmac_f32_e32 v157, v139, v115
	v_fmac_f32_e32 v158, v154, v115
	v_fmac_f32_e32 v159, v155, v115
	v_add_f32_e32 v186, v186, v156
	v_add_f32_e32 v187, v187, v157
	v_add_f32_e32 v188, v188, v158
	v_add_f32_e32 v189, v189, v159
	s_waitcnt vmcnt(29)
	v_cvt_f32_ubyte0_e32 v124, v48
	v_cvt_f32_ubyte1_e32 v126, v48
	v_cvt_f32_ubyte2_e32 v128, v48
	v_cvt_f32_ubyte3_e32 v130, v48
	v_cvt_f32_ubyte0_e32 v132, v49
	v_cvt_f32_ubyte1_e32 v134, v49
	v_cvt_f32_ubyte2_e32 v136, v49
	v_cvt_f32_ubyte3_e32 v138, v49
	s_lshl_b32 s30, s80, 12
	s_add_u32 s28, s26, s30
	s_addc_u32 s29, s27, 0
	global_load_dwordx2 v[48:49], v162, s[28:29]
	v_cvt_f32_ubyte0_e32 v125, v50
	v_cvt_f32_ubyte1_e32 v127, v50
	v_cvt_f32_ubyte2_e32 v129, v50
	v_cvt_f32_ubyte3_e32 v131, v50
	v_cvt_f32_ubyte0_e32 v133, v51
	v_cvt_f32_ubyte1_e32 v135, v51
	v_cvt_f32_ubyte2_e32 v137, v51
	v_cvt_f32_ubyte3_e32 v139, v51
	s_lshl_b32 s30, s81, 12
	s_add_u32 s28, s26, s30
	s_addc_u32 s29, s27, 0
	global_load_dwordx2 v[50:51], v162, s[28:29]
	v_cvt_f32_ubyte0_e32 v140, v52
	v_cvt_f32_ubyte1_e32 v142, v52
	v_cvt_f32_ubyte2_e32 v144, v52
	v_cvt_f32_ubyte3_e32 v146, v52
	v_cvt_f32_ubyte0_e32 v148, v53
	v_cvt_f32_ubyte1_e32 v150, v53
	v_cvt_f32_ubyte2_e32 v152, v53
	v_cvt_f32_ubyte3_e32 v154, v53
	s_lshl_b32 s30, s82, 12
	s_add_u32 s28, s26, s30
	s_addc_u32 s29, s27, 0
	global_load_dwordx2 v[52:53], v162, s[28:29]
	v_cvt_f32_ubyte0_e32 v141, v54
	v_cvt_f32_ubyte1_e32 v143, v54
	v_cvt_f32_ubyte2_e32 v145, v54
	v_cvt_f32_ubyte3_e32 v147, v54
	v_cvt_f32_ubyte0_e32 v149, v55
	v_cvt_f32_ubyte1_e32 v151, v55
	v_cvt_f32_ubyte2_e32 v153, v55
	v_cvt_f32_ubyte3_e32 v155, v55
	s_lshl_b32 s30, s83, 12
	s_add_u32 s28, s26, s30
	s_addc_u32 s29, s27, 0
	global_load_dwordx2 v[54:55], v162, s[28:29]
	v_mul_f32_e32 v190, v124, v108
	v_mul_f32_e32 v191, v125, v108
	v_mul_f32_e32 v192, v140, v108
	v_mul_f32_e32 v193, v141, v108
	v_mul_f32_e32 v156, v126, v109
	v_mul_f32_e32 v157, v127, v109
	v_mul_f32_e32 v158, v142, v109
	v_mul_f32_e32 v159, v143, v109
	v_fmac_f32_e32 v190, v128, v110
	v_fmac_f32_e32 v191, v129, v110
	v_fmac_f32_e32 v192, v144, v110
	v_fmac_f32_e32 v193, v145, v110
	v_fmac_f32_e32 v156, v130, v111
	v_fmac_f32_e32 v157, v131, v111
	v_fmac_f32_e32 v158, v146, v111
	v_fmac_f32_e32 v159, v147, v111
	v_fmac_f32_e32 v190, v132, v112
	v_fmac_f32_e32 v191, v133, v112
	v_fmac_f32_e32 v192, v148, v112
	v_fmac_f32_e32 v193, v149, v112
	v_fmac_f32_e32 v156, v134, v113
	v_fmac_f32_e32 v157, v135, v113
	v_fmac_f32_e32 v158, v150, v113
	v_fmac_f32_e32 v159, v151, v113
	v_fmac_f32_e32 v190, v136, v114
	v_fmac_f32_e32 v191, v137, v114
	v_fmac_f32_e32 v192, v152, v114
	v_fmac_f32_e32 v193, v153, v114
	v_fmac_f32_e32 v156, v138, v115
	v_fmac_f32_e32 v157, v139, v115
	v_fmac_f32_e32 v158, v154, v115
	v_fmac_f32_e32 v159, v155, v115
	v_add_f32_e32 v190, v190, v156
	v_add_f32_e32 v191, v191, v157
	v_add_f32_e32 v192, v192, v158
	v_add_f32_e32 v193, v193, v159
	s_waitcnt vmcnt(29)
	v_cvt_f32_ubyte0_e32 v124, v56
	v_cvt_f32_ubyte1_e32 v126, v56
	v_cvt_f32_ubyte2_e32 v128, v56
	v_cvt_f32_ubyte3_e32 v130, v56
	v_cvt_f32_ubyte0_e32 v132, v57
	v_cvt_f32_ubyte1_e32 v134, v57
	v_cvt_f32_ubyte2_e32 v136, v57
	v_cvt_f32_ubyte3_e32 v138, v57
	s_waitcnt lgkmcnt(0)
	s_load_dwordx16 s[68:83], s[36:37], 0x180 glc
	s_lshl_b32 s30, s84, 12
	s_add_u32 s28, s26, s30
	s_addc_u32 s29, s27, 0
	global_load_dwordx2 v[56:57], v162, s[28:29]
	v_cvt_f32_ubyte0_e32 v125, v58
	v_cvt_f32_ubyte1_e32 v127, v58
	v_cvt_f32_ubyte2_e32 v129, v58
	v_cvt_f32_ubyte3_e32 v131, v58
	v_cvt_f32_ubyte0_e32 v133, v59
	v_cvt_f32_ubyte1_e32 v135, v59
	v_cvt_f32_ubyte2_e32 v137, v59
	v_cvt_f32_ubyte3_e32 v139, v59
	s_lshl_b32 s30, s85, 12
	s_add_u32 s28, s26, s30
	s_addc_u32 s29, s27, 0
	global_load_dwordx2 v[58:59], v162, s[28:29]
	v_cvt_f32_ubyte0_e32 v140, v60
	v_cvt_f32_ubyte1_e32 v142, v60
	v_cvt_f32_ubyte2_e32 v144, v60
	v_cvt_f32_ubyte3_e32 v146, v60
	v_cvt_f32_ubyte0_e32 v148, v61
	v_cvt_f32_ubyte1_e32 v150, v61
	v_cvt_f32_ubyte2_e32 v152, v61
	v_cvt_f32_ubyte3_e32 v154, v61
	s_lshl_b32 s30, s86, 12
	s_add_u32 s28, s26, s30
	s_addc_u32 s29, s27, 0
	global_load_dwordx2 v[60:61], v162, s[28:29]
	v_cvt_f32_ubyte0_e32 v141, v62
	v_cvt_f32_ubyte1_e32 v143, v62
	v_cvt_f32_ubyte2_e32 v145, v62
	v_cvt_f32_ubyte3_e32 v147, v62
	v_cvt_f32_ubyte0_e32 v149, v63
	v_cvt_f32_ubyte1_e32 v151, v63
	v_cvt_f32_ubyte2_e32 v153, v63
	v_cvt_f32_ubyte3_e32 v155, v63
	s_lshl_b32 s30, s87, 12
	s_add_u32 s28, s26, s30
	s_addc_u32 s29, s27, 0
	global_load_dwordx2 v[62:63], v162, s[28:29]
	v_mul_f32_e32 v194, v124, v108
	v_mul_f32_e32 v195, v125, v108
	v_mul_f32_e32 v196, v140, v108
	v_mul_f32_e32 v197, v141, v108
	v_mul_f32_e32 v156, v126, v109
	v_mul_f32_e32 v157, v127, v109
	v_mul_f32_e32 v158, v142, v109
	v_mul_f32_e32 v159, v143, v109
	v_fmac_f32_e32 v194, v128, v110
	v_fmac_f32_e32 v195, v129, v110
	v_fmac_f32_e32 v196, v144, v110
	v_fmac_f32_e32 v197, v145, v110
	v_fmac_f32_e32 v156, v130, v111
	v_fmac_f32_e32 v157, v131, v111
	v_fmac_f32_e32 v158, v146, v111
	v_fmac_f32_e32 v159, v147, v111
	v_fmac_f32_e32 v194, v132, v112
	v_fmac_f32_e32 v195, v133, v112
	v_fmac_f32_e32 v196, v148, v112
	v_fmac_f32_e32 v197, v149, v112
	v_fmac_f32_e32 v156, v134, v113
	v_fmac_f32_e32 v157, v135, v113
	v_fmac_f32_e32 v158, v150, v113
	v_fmac_f32_e32 v159, v151, v113
	v_fmac_f32_e32 v194, v136, v114
	v_fmac_f32_e32 v195, v137, v114
	v_fmac_f32_e32 v196, v152, v114
	v_fmac_f32_e32 v197, v153, v114
	v_fmac_f32_e32 v156, v138, v115
	v_fmac_f32_e32 v157, v139, v115
	v_fmac_f32_e32 v158, v154, v115
	v_fmac_f32_e32 v159, v155, v115
	v_add_f32_e32 v194, v194, v156
	v_add_f32_e32 v195, v195, v157
	v_add_f32_e32 v196, v196, v158
	v_add_f32_e32 v197, v197, v159
	s_waitcnt vmcnt(29)
	v_cvt_f32_ubyte0_e32 v124, v64
	v_cvt_f32_ubyte1_e32 v126, v64
	v_cvt_f32_ubyte2_e32 v128, v64
	v_cvt_f32_ubyte3_e32 v130, v64
	v_cvt_f32_ubyte0_e32 v132, v65
	v_cvt_f32_ubyte1_e32 v134, v65
	v_cvt_f32_ubyte2_e32 v136, v65
	v_cvt_f32_ubyte3_e32 v138, v65
	s_lshl_b32 s30, s88, 12
	s_add_u32 s28, s26, s30
	s_addc_u32 s29, s27, 0
	global_load_dwordx2 v[64:65], v162, s[28:29]
	v_cvt_f32_ubyte0_e32 v125, v66
	v_cvt_f32_ubyte1_e32 v127, v66
	v_cvt_f32_ubyte2_e32 v129, v66
	v_cvt_f32_ubyte3_e32 v131, v66
	v_cvt_f32_ubyte0_e32 v133, v67
	v_cvt_f32_ubyte1_e32 v135, v67
	v_cvt_f32_ubyte2_e32 v137, v67
	v_cvt_f32_ubyte3_e32 v139, v67
	s_lshl_b32 s30, s89, 12
	s_add_u32 s28, s26, s30
	s_addc_u32 s29, s27, 0
	global_load_dwordx2 v[66:67], v162, s[28:29]
	v_cvt_f32_ubyte0_e32 v140, v68
	v_cvt_f32_ubyte1_e32 v142, v68
	v_cvt_f32_ubyte2_e32 v144, v68
	v_cvt_f32_ubyte3_e32 v146, v68
	v_cvt_f32_ubyte0_e32 v148, v69
	v_cvt_f32_ubyte1_e32 v150, v69
	v_cvt_f32_ubyte2_e32 v152, v69
	v_cvt_f32_ubyte3_e32 v154, v69
	s_lshl_b32 s30, s90, 12
	s_add_u32 s28, s26, s30
	s_addc_u32 s29, s27, 0
	global_load_dwordx2 v[68:69], v162, s[28:29]
	v_cvt_f32_ubyte0_e32 v141, v70
	v_cvt_f32_ubyte1_e32 v143, v70
	v_cvt_f32_ubyte2_e32 v145, v70
	v_cvt_f32_ubyte3_e32 v147, v70
	v_cvt_f32_ubyte0_e32 v149, v71
	v_cvt_f32_ubyte1_e32 v151, v71
	v_cvt_f32_ubyte2_e32 v153, v71
	v_cvt_f32_ubyte3_e32 v155, v71
	s_lshl_b32 s30, s91, 12
	s_add_u32 s28, s26, s30
	s_addc_u32 s29, s27, 0
	global_load_dwordx2 v[70:71], v162, s[28:29]
	v_mul_f32_e32 v198, v124, v108
	v_mul_f32_e32 v199, v125, v108
	v_mul_f32_e32 v200, v140, v108
	v_mul_f32_e32 v201, v141, v108
	v_mul_f32_e32 v156, v126, v109
	v_mul_f32_e32 v157, v127, v109
	v_mul_f32_e32 v158, v142, v109
	v_mul_f32_e32 v159, v143, v109
	v_fmac_f32_e32 v198, v128, v110
	v_fmac_f32_e32 v199, v129, v110
	v_fmac_f32_e32 v200, v144, v110
	v_fmac_f32_e32 v201, v145, v110
	v_fmac_f32_e32 v156, v130, v111
	v_fmac_f32_e32 v157, v131, v111
	v_fmac_f32_e32 v158, v146, v111
	v_fmac_f32_e32 v159, v147, v111
	v_fmac_f32_e32 v198, v132, v112
	v_fmac_f32_e32 v199, v133, v112
	v_fmac_f32_e32 v200, v148, v112
	v_fmac_f32_e32 v201, v149, v112
	v_fmac_f32_e32 v156, v134, v113
	v_fmac_f32_e32 v157, v135, v113
	v_fmac_f32_e32 v158, v150, v113
	v_fmac_f32_e32 v159, v151, v113
	v_fmac_f32_e32 v198, v136, v114
	v_fmac_f32_e32 v199, v137, v114
	v_fmac_f32_e32 v200, v152, v114
	v_fmac_f32_e32 v201, v153, v114
	v_fmac_f32_e32 v156, v138, v115
	v_fmac_f32_e32 v157, v139, v115
	v_fmac_f32_e32 v158, v154, v115
	v_fmac_f32_e32 v159, v155, v115
	v_add_f32_e32 v198, v198, v156
	v_add_f32_e32 v199, v199, v157
	v_add_f32_e32 v200, v200, v158
	v_add_f32_e32 v201, v201, v159
	s_waitcnt vmcnt(29)
	v_cvt_f32_ubyte0_e32 v124, v72
	v_cvt_f32_ubyte1_e32 v126, v72
	v_cvt_f32_ubyte2_e32 v128, v72
	v_cvt_f32_ubyte3_e32 v130, v72
	v_cvt_f32_ubyte0_e32 v132, v73
	v_cvt_f32_ubyte1_e32 v134, v73
	v_cvt_f32_ubyte2_e32 v136, v73
	v_cvt_f32_ubyte3_e32 v138, v73
	s_lshl_b32 s30, s92, 12
	s_add_u32 s28, s26, s30
	s_addc_u32 s29, s27, 0
	global_load_dwordx2 v[72:73], v162, s[28:29]
	v_cvt_f32_ubyte0_e32 v125, v74
	v_cvt_f32_ubyte1_e32 v127, v74
	v_cvt_f32_ubyte2_e32 v129, v74
	v_cvt_f32_ubyte3_e32 v131, v74
	v_cvt_f32_ubyte0_e32 v133, v75
	v_cvt_f32_ubyte1_e32 v135, v75
	v_cvt_f32_ubyte2_e32 v137, v75
	v_cvt_f32_ubyte3_e32 v139, v75
	s_lshl_b32 s30, s93, 12
	s_add_u32 s28, s26, s30
	s_addc_u32 s29, s27, 0
	global_load_dwordx2 v[74:75], v162, s[28:29]
	v_cvt_f32_ubyte0_e32 v140, v76
	v_cvt_f32_ubyte1_e32 v142, v76
	v_cvt_f32_ubyte2_e32 v144, v76
	v_cvt_f32_ubyte3_e32 v146, v76
	v_cvt_f32_ubyte0_e32 v148, v77
	v_cvt_f32_ubyte1_e32 v150, v77
	v_cvt_f32_ubyte2_e32 v152, v77
	v_cvt_f32_ubyte3_e32 v154, v77
	s_lshl_b32 s30, s94, 12
	s_add_u32 s28, s26, s30
	s_addc_u32 s29, s27, 0
	global_load_dwordx2 v[76:77], v162, s[28:29]
	v_cvt_f32_ubyte0_e32 v141, v78
	v_cvt_f32_ubyte1_e32 v143, v78
	v_cvt_f32_ubyte2_e32 v145, v78
	v_cvt_f32_ubyte3_e32 v147, v78
	v_cvt_f32_ubyte0_e32 v149, v79
	v_cvt_f32_ubyte1_e32 v151, v79
	v_cvt_f32_ubyte2_e32 v153, v79
	v_cvt_f32_ubyte3_e32 v155, v79
	s_lshl_b32 s30, s95, 12
	s_add_u32 s28, s26, s30
	s_addc_u32 s29, s27, 0
	global_load_dwordx2 v[78:79], v162, s[28:29]
	v_mul_f32_e32 v202, v124, v108
	v_mul_f32_e32 v203, v125, v108
	v_mul_f32_e32 v204, v140, v108
	v_mul_f32_e32 v205, v141, v108
	v_mul_f32_e32 v156, v126, v109
	v_mul_f32_e32 v157, v127, v109
	v_mul_f32_e32 v158, v142, v109
	v_mul_f32_e32 v159, v143, v109
	v_fmac_f32_e32 v202, v128, v110
	v_fmac_f32_e32 v203, v129, v110
	v_fmac_f32_e32 v204, v144, v110
	v_fmac_f32_e32 v205, v145, v110
	v_fmac_f32_e32 v156, v130, v111
	v_fmac_f32_e32 v157, v131, v111
	v_fmac_f32_e32 v158, v146, v111
	v_fmac_f32_e32 v159, v147, v111
	v_fmac_f32_e32 v202, v132, v112
	v_fmac_f32_e32 v203, v133, v112
	v_fmac_f32_e32 v204, v148, v112
	v_fmac_f32_e32 v205, v149, v112
	v_fmac_f32_e32 v156, v134, v113
	v_fmac_f32_e32 v157, v135, v113
	v_fmac_f32_e32 v158, v150, v113
	v_fmac_f32_e32 v159, v151, v113
	v_fmac_f32_e32 v202, v136, v114
	v_fmac_f32_e32 v203, v137, v114
	v_fmac_f32_e32 v204, v152, v114
	v_fmac_f32_e32 v205, v153, v114
	v_fmac_f32_e32 v156, v138, v115
	v_fmac_f32_e32 v157, v139, v115
	v_fmac_f32_e32 v158, v154, v115
	v_fmac_f32_e32 v159, v155, v115
	v_add_f32_e32 v202, v202, v156
	v_add_f32_e32 v203, v203, v157
	v_add_f32_e32 v204, v204, v158
	v_add_f32_e32 v205, v205, v159
	s_waitcnt vmcnt(29)
	v_cvt_f32_ubyte0_e32 v124, v80
	v_cvt_f32_ubyte1_e32 v126, v80
	v_cvt_f32_ubyte2_e32 v128, v80
	v_cvt_f32_ubyte3_e32 v130, v80
	v_cvt_f32_ubyte0_e32 v132, v81
	v_cvt_f32_ubyte1_e32 v134, v81
	v_cvt_f32_ubyte2_e32 v136, v81
	v_cvt_f32_ubyte3_e32 v138, v81
	s_lshl_b32 s30, s96, 12
	s_add_u32 s28, s26, s30
	s_addc_u32 s29, s27, 0
	global_load_dwordx2 v[80:81], v162, s[28:29]
	v_cvt_f32_ubyte0_e32 v125, v82
	v_cvt_f32_ubyte1_e32 v127, v82
	v_cvt_f32_ubyte2_e32 v129, v82
	v_cvt_f32_ubyte3_e32 v131, v82
	v_cvt_f32_ubyte0_e32 v133, v83
	v_cvt_f32_ubyte1_e32 v135, v83
	v_cvt_f32_ubyte2_e32 v137, v83
	v_cvt_f32_ubyte3_e32 v139, v83
	s_lshl_b32 s30, s97, 12
	s_add_u32 s28, s26, s30
	s_addc_u32 s29, s27, 0
	global_load_dwordx2 v[82:83], v162, s[28:29]
	v_cvt_f32_ubyte0_e32 v140, v84
	v_cvt_f32_ubyte1_e32 v142, v84
	v_cvt_f32_ubyte2_e32 v144, v84
	v_cvt_f32_ubyte3_e32 v146, v84
	v_cvt_f32_ubyte0_e32 v148, v85
	v_cvt_f32_ubyte1_e32 v150, v85
	v_cvt_f32_ubyte2_e32 v152, v85
	v_cvt_f32_ubyte3_e32 v154, v85
	s_lshl_b32 s30, s98, 12
	s_add_u32 s28, s26, s30
	s_addc_u32 s29, s27, 0
	global_load_dwordx2 v[84:85], v162, s[28:29]
	v_cvt_f32_ubyte0_e32 v141, v86
	v_cvt_f32_ubyte1_e32 v143, v86
	v_cvt_f32_ubyte2_e32 v145, v86
	v_cvt_f32_ubyte3_e32 v147, v86
	v_cvt_f32_ubyte0_e32 v149, v87
	v_cvt_f32_ubyte1_e32 v151, v87
	v_cvt_f32_ubyte2_e32 v153, v87
	v_cvt_f32_ubyte3_e32 v155, v87
	s_lshl_b32 s30, s99, 12
	s_add_u32 s28, s26, s30
	s_addc_u32 s29, s27, 0
	global_load_dwordx2 v[86:87], v162, s[28:29]
	v_mul_f32_e32 v206, v124, v108
	v_mul_f32_e32 v207, v125, v108
	v_mul_f32_e32 v208, v140, v108
	v_mul_f32_e32 v209, v141, v108
	v_mul_f32_e32 v156, v126, v109
	v_mul_f32_e32 v157, v127, v109
	v_mul_f32_e32 v158, v142, v109
	v_mul_f32_e32 v159, v143, v109
	v_fmac_f32_e32 v206, v128, v110
	v_fmac_f32_e32 v207, v129, v110
	v_fmac_f32_e32 v208, v144, v110
	v_fmac_f32_e32 v209, v145, v110
	v_fmac_f32_e32 v156, v130, v111
	v_fmac_f32_e32 v157, v131, v111
	v_fmac_f32_e32 v158, v146, v111
	v_fmac_f32_e32 v159, v147, v111
	v_fmac_f32_e32 v206, v132, v112
	v_fmac_f32_e32 v207, v133, v112
	v_fmac_f32_e32 v208, v148, v112
	v_fmac_f32_e32 v209, v149, v112
	v_fmac_f32_e32 v156, v134, v113
	v_fmac_f32_e32 v157, v135, v113
	v_fmac_f32_e32 v158, v150, v113
	v_fmac_f32_e32 v159, v151, v113
	v_fmac_f32_e32 v206, v136, v114
	v_fmac_f32_e32 v207, v137, v114
	v_fmac_f32_e32 v208, v152, v114
	v_fmac_f32_e32 v209, v153, v114
	v_fmac_f32_e32 v156, v138, v115
	v_fmac_f32_e32 v157, v139, v115
	v_fmac_f32_e32 v158, v154, v115
	v_fmac_f32_e32 v159, v155, v115
	v_add_f32_e32 v206, v206, v156
	v_add_f32_e32 v207, v207, v157
	v_add_f32_e32 v208, v208, v158
	v_add_f32_e32 v209, v209, v159
	v_permlane32_swap_b32_e32 v178, v194
	v_permlane32_swap_b32_e32 v179, v195
	v_permlane32_swap_b32_e32 v180, v196
	v_permlane32_swap_b32_e32 v181, v197
	v_permlane32_swap_b32_e32 v182, v198
	v_permlane32_swap_b32_e32 v183, v199
	v_permlane32_swap_b32_e32 v184, v200
	v_permlane32_swap_b32_e32 v185, v201
	v_permlane32_swap_b32_e32 v186, v202
	v_permlane32_swap_b32_e32 v187, v203
	v_permlane32_swap_b32_e32 v188, v204
	v_permlane32_swap_b32_e32 v189, v205
	v_permlane32_swap_b32_e32 v190, v206
	v_permlane32_swap_b32_e32 v191, v207
	v_permlane32_swap_b32_e32 v192, v208
	v_permlane32_swap_b32_e32 v193, v209
	v_add_f32_e32 v178, v178, v194
	v_add_f32_e32 v179, v179, v195
	v_add_f32_e32 v180, v180, v196
	v_add_f32_e32 v181, v181, v197
	v_add_f32_e32 v182, v182, v198
	v_add_f32_e32 v183, v183, v199
	v_add_f32_e32 v184, v184, v200
	v_add_f32_e32 v185, v185, v201
	v_add_f32_e32 v186, v186, v202
	v_add_f32_e32 v187, v187, v203
	v_add_f32_e32 v188, v188, v204
	v_add_f32_e32 v189, v189, v205
	v_add_f32_e32 v190, v190, v206
	v_add_f32_e32 v191, v191, v207
	v_add_f32_e32 v192, v192, v208
	v_add_f32_e32 v193, v193, v209
	v_permlane16_swap_b32_e32 v178, v186
	v_permlane16_swap_b32_e32 v179, v187
	v_permlane16_swap_b32_e32 v180, v188
	v_permlane16_swap_b32_e32 v181, v189
	v_permlane16_swap_b32_e32 v182, v190
	v_permlane16_swap_b32_e32 v183, v191
	v_permlane16_swap_b32_e32 v184, v192
	v_permlane16_swap_b32_e32 v185, v193
	v_add_f32_e32 v178, v178, v186
	v_add_f32_e32 v179, v179, v187
	v_add_f32_e32 v180, v180, v188
	v_add_f32_e32 v181, v181, v189
	v_add_f32_e32 v182, v182, v190
	v_add_f32_e32 v183, v183, v191
	v_add_f32_e32 v184, v184, v192
	v_add_f32_e32 v185, v185, v193
	v_cndmask_b32_e64 v2, v178, v182, s[8:9]
	v_cndmask_b32_e64 v3, v179, v183, s[8:9]
	v_cndmask_b32_e64 v4, v180, v184, s[8:9]
	v_cndmask_b32_e64 v5, v181, v185, s[8:9]
	v_cndmask_b32_e64 v6, v182, v178, s[8:9]
	v_cndmask_b32_e64 v7, v183, v179, s[8:9]
	v_cndmask_b32_e64 v8, v184, v180, s[8:9]
	v_cndmask_b32_e64 v9, v185, v181, s[8:9]
	v_add_f32_dpp v6, v2, v6 row_ror:8 row_mask:0xf bank_mask:0xf
	v_add_f32_dpp v7, v3, v7 row_ror:8 row_mask:0xf bank_mask:0xf
	v_add_f32_dpp v8, v4, v8 row_ror:8 row_mask:0xf bank_mask:0xf
	v_add_f32_dpp v9, v5, v9 row_ror:8 row_mask:0xf bank_mask:0xf
	v_cndmask_b32_e64 v2, v6, v8, s[10:11]
	v_cndmask_b32_e64 v3, v7, v9, s[10:11]
	v_cndmask_b32_e64 v4, v8, v6, s[10:11]
	v_cndmask_b32_e64 v5, v9, v7, s[10:11]
	v_add_f32_dpp v4, v2, v4 row_half_mirror row_mask:0xf bank_mask:0xf
	v_add_f32_dpp v5, v3, v5 row_half_mirror row_mask:0xf bank_mask:0xf
	v_cndmask_b32_e64 v2, v4, v5, s[14:15]
	v_cndmask_b32_e64 v3, v5, v4, s[14:15]
	s_nop 0
	v_add_f32_dpp v3, v2, v3 quad_perm:[2,3,0,1] row_mask:0xf bank_mask:0xf
	s_nop 1
	v_add_f32_dpp v11, v3, v3 quad_perm:[1,0,3,2] row_mask:0xf bank_mask:0xf
	s_mov_b64 exec, s[2:3]
	global_store_dword v[22:23], v11, off offset:128
	s_mov_b64 exec, -1
	s_waitcnt vmcnt(29)
	v_cvt_f32_ubyte0_e32 v124, v24
	v_cvt_f32_ubyte1_e32 v126, v24
	v_cvt_f32_ubyte2_e32 v128, v24
	v_cvt_f32_ubyte3_e32 v130, v24
	v_cvt_f32_ubyte0_e32 v132, v25
	v_cvt_f32_ubyte1_e32 v134, v25
	v_cvt_f32_ubyte2_e32 v136, v25
	v_cvt_f32_ubyte3_e32 v138, v25
	s_waitcnt lgkmcnt(0)
	s_load_dwordx16 s[84:99], s[36:37], 0x1c0 glc
	s_lshl_b32 s30, s68, 12
	s_add_u32 s28, s26, s30
	s_addc_u32 s29, s27, 0
	global_load_dwordx2 v[24:25], v162, s[28:29]
	v_cvt_f32_ubyte0_e32 v125, v26
	v_cvt_f32_ubyte1_e32 v127, v26
	v_cvt_f32_ubyte2_e32 v129, v26
	v_cvt_f32_ubyte3_e32 v131, v26
	v_cvt_f32_ubyte0_e32 v133, v27
	v_cvt_f32_ubyte1_e32 v135, v27
	v_cvt_f32_ubyte2_e32 v137, v27
	v_cvt_f32_ubyte3_e32 v139, v27
	s_lshl_b32 s30, s69, 12
	s_add_u32 s28, s26, s30
	s_addc_u32 s29, s27, 0
	global_load_dwordx2 v[26:27], v162, s[28:29]
	v_cvt_f32_ubyte0_e32 v140, v28
	v_cvt_f32_ubyte1_e32 v142, v28
	v_cvt_f32_ubyte2_e32 v144, v28
	v_cvt_f32_ubyte3_e32 v146, v28
	v_cvt_f32_ubyte0_e32 v148, v29
	v_cvt_f32_ubyte1_e32 v150, v29
	v_cvt_f32_ubyte2_e32 v152, v29
	v_cvt_f32_ubyte3_e32 v154, v29
	s_lshl_b32 s30, s70, 12
	s_add_u32 s28, s26, s30
	s_addc_u32 s29, s27, 0
	global_load_dwordx2 v[28:29], v162, s[28:29]
	v_cvt_f32_ubyte0_e32 v141, v30
	v_cvt_f32_ubyte1_e32 v143, v30
	v_cvt_f32_ubyte2_e32 v145, v30
	v_cvt_f32_ubyte3_e32 v147, v30
	v_cvt_f32_ubyte0_e32 v149, v31
	v_cvt_f32_ubyte1_e32 v151, v31
	v_cvt_f32_ubyte2_e32 v153, v31
	v_cvt_f32_ubyte3_e32 v155, v31
	s_lshl_b32 s30, s71, 12
	s_add_u32 s28, s26, s30
	s_addc_u32 s29, s27, 0
	global_load_dwordx2 v[30:31], v162, s[28:29]
	v_mul_f32_e32 v178, v124, v108
	v_mul_f32_e32 v179, v125, v108
	v_mul_f32_e32 v180, v140, v108
	v_mul_f32_e32 v181, v141, v108
	v_mul_f32_e32 v156, v126, v109
	v_mul_f32_e32 v157, v127, v109
	v_mul_f32_e32 v158, v142, v109
	v_mul_f32_e32 v159, v143, v109
	v_fmac_f32_e32 v178, v128, v110
	v_fmac_f32_e32 v179, v129, v110
	v_fmac_f32_e32 v180, v144, v110
	v_fmac_f32_e32 v181, v145, v110
	v_fmac_f32_e32 v156, v130, v111
	v_fmac_f32_e32 v157, v131, v111
	v_fmac_f32_e32 v158, v146, v111
	v_fmac_f32_e32 v159, v147, v111
	v_fmac_f32_e32 v178, v132, v112
	v_fmac_f32_e32 v179, v133, v112
	v_fmac_f32_e32 v180, v148, v112
	v_fmac_f32_e32 v181, v149, v112
	v_fmac_f32_e32 v156, v134, v113
	v_fmac_f32_e32 v157, v135, v113
	v_fmac_f32_e32 v158, v150, v113
	v_fmac_f32_e32 v159, v151, v113
	v_fmac_f32_e32 v178, v136, v114
	v_fmac_f32_e32 v179, v137, v114
	v_fmac_f32_e32 v180, v152, v114
	v_fmac_f32_e32 v181, v153, v114
	v_fmac_f32_e32 v156, v138, v115
	v_fmac_f32_e32 v157, v139, v115
	v_fmac_f32_e32 v158, v154, v115
	v_fmac_f32_e32 v159, v155, v115
	v_add_f32_e32 v178, v178, v156
	v_add_f32_e32 v179, v179, v157
	v_add_f32_e32 v180, v180, v158
	v_add_f32_e32 v181, v181, v159
	s_waitcnt vmcnt(29)
	v_cvt_f32_ubyte0_e32 v124, v32
	v_cvt_f32_ubyte1_e32 v126, v32
	v_cvt_f32_ubyte2_e32 v128, v32
	v_cvt_f32_ubyte3_e32 v130, v32
	v_cvt_f32_ubyte0_e32 v132, v33
	v_cvt_f32_ubyte1_e32 v134, v33
	v_cvt_f32_ubyte2_e32 v136, v33
	v_cvt_f32_ubyte3_e32 v138, v33
	s_lshl_b32 s30, s72, 12
	s_add_u32 s28, s26, s30
	s_addc_u32 s29, s27, 0
	global_load_dwordx2 v[32:33], v162, s[28:29]
	v_cvt_f32_ubyte0_e32 v125, v34
	v_cvt_f32_ubyte1_e32 v127, v34
	v_cvt_f32_ubyte2_e32 v129, v34
	v_cvt_f32_ubyte3_e32 v131, v34
	v_cvt_f32_ubyte0_e32 v133, v35
	v_cvt_f32_ubyte1_e32 v135, v35
	v_cvt_f32_ubyte2_e32 v137, v35
	v_cvt_f32_ubyte3_e32 v139, v35
	s_lshl_b32 s30, s73, 12
	s_add_u32 s28, s26, s30
	s_addc_u32 s29, s27, 0
	global_load_dwordx2 v[34:35], v162, s[28:29]
	v_cvt_f32_ubyte0_e32 v140, v36
	v_cvt_f32_ubyte1_e32 v142, v36
	v_cvt_f32_ubyte2_e32 v144, v36
	v_cvt_f32_ubyte3_e32 v146, v36
	v_cvt_f32_ubyte0_e32 v148, v37
	v_cvt_f32_ubyte1_e32 v150, v37
	v_cvt_f32_ubyte2_e32 v152, v37
	v_cvt_f32_ubyte3_e32 v154, v37
	s_lshl_b32 s30, s74, 12
	s_add_u32 s28, s26, s30
	s_addc_u32 s29, s27, 0
	global_load_dwordx2 v[36:37], v162, s[28:29]
	v_cvt_f32_ubyte0_e32 v141, v38
	v_cvt_f32_ubyte1_e32 v143, v38
	v_cvt_f32_ubyte2_e32 v145, v38
	v_cvt_f32_ubyte3_e32 v147, v38
	v_cvt_f32_ubyte0_e32 v149, v39
	v_cvt_f32_ubyte1_e32 v151, v39
	v_cvt_f32_ubyte2_e32 v153, v39
	v_cvt_f32_ubyte3_e32 v155, v39
	s_lshl_b32 s30, s75, 12
	s_add_u32 s28, s26, s30
	s_addc_u32 s29, s27, 0
	global_load_dwordx2 v[38:39], v162, s[28:29]
	v_mul_f32_e32 v182, v124, v108
	v_mul_f32_e32 v183, v125, v108
	v_mul_f32_e32 v184, v140, v108
	v_mul_f32_e32 v185, v141, v108
	v_mul_f32_e32 v156, v126, v109
	v_mul_f32_e32 v157, v127, v109
	v_mul_f32_e32 v158, v142, v109
	v_mul_f32_e32 v159, v143, v109
	v_fmac_f32_e32 v182, v128, v110
	v_fmac_f32_e32 v183, v129, v110
	v_fmac_f32_e32 v184, v144, v110
	v_fmac_f32_e32 v185, v145, v110
	v_fmac_f32_e32 v156, v130, v111
	v_fmac_f32_e32 v157, v131, v111
	v_fmac_f32_e32 v158, v146, v111
	v_fmac_f32_e32 v159, v147, v111
	v_fmac_f32_e32 v182, v132, v112
	v_fmac_f32_e32 v183, v133, v112
	v_fmac_f32_e32 v184, v148, v112
	v_fmac_f32_e32 v185, v149, v112
	v_fmac_f32_e32 v156, v134, v113
	v_fmac_f32_e32 v157, v135, v113
	v_fmac_f32_e32 v158, v150, v113
	v_fmac_f32_e32 v159, v151, v113
	v_fmac_f32_e32 v182, v136, v114
	v_fmac_f32_e32 v183, v137, v114
	v_fmac_f32_e32 v184, v152, v114
	v_fmac_f32_e32 v185, v153, v114
	v_fmac_f32_e32 v156, v138, v115
	v_fmac_f32_e32 v157, v139, v115
	v_fmac_f32_e32 v158, v154, v115
	v_fmac_f32_e32 v159, v155, v115
	v_add_f32_e32 v182, v182, v156
	v_add_f32_e32 v183, v183, v157
	v_add_f32_e32 v184, v184, v158
	v_add_f32_e32 v185, v185, v159
	s_waitcnt vmcnt(29)
	v_cvt_f32_ubyte0_e32 v124, v40
	v_cvt_f32_ubyte1_e32 v126, v40
	v_cvt_f32_ubyte2_e32 v128, v40
	v_cvt_f32_ubyte3_e32 v130, v40
	v_cvt_f32_ubyte0_e32 v132, v41
	v_cvt_f32_ubyte1_e32 v134, v41
	v_cvt_f32_ubyte2_e32 v136, v41
	v_cvt_f32_ubyte3_e32 v138, v41
	s_lshl_b32 s30, s76, 12
	s_add_u32 s28, s26, s30
	s_addc_u32 s29, s27, 0
	global_load_dwordx2 v[40:41], v162, s[28:29]
	v_cvt_f32_ubyte0_e32 v125, v42
	v_cvt_f32_ubyte1_e32 v127, v42
	v_cvt_f32_ubyte2_e32 v129, v42
	v_cvt_f32_ubyte3_e32 v131, v42
	v_cvt_f32_ubyte0_e32 v133, v43
	v_cvt_f32_ubyte1_e32 v135, v43
	v_cvt_f32_ubyte2_e32 v137, v43
	v_cvt_f32_ubyte3_e32 v139, v43
	s_lshl_b32 s30, s77, 12
	s_add_u32 s28, s26, s30
	s_addc_u32 s29, s27, 0
	global_load_dwordx2 v[42:43], v162, s[28:29]
	v_cvt_f32_ubyte0_e32 v140, v44
	v_cvt_f32_ubyte1_e32 v142, v44
	v_cvt_f32_ubyte2_e32 v144, v44
	v_cvt_f32_ubyte3_e32 v146, v44
	v_cvt_f32_ubyte0_e32 v148, v45
	v_cvt_f32_ubyte1_e32 v150, v45
	v_cvt_f32_ubyte2_e32 v152, v45
	v_cvt_f32_ubyte3_e32 v154, v45
	s_lshl_b32 s30, s78, 12
	s_add_u32 s28, s26, s30
	s_addc_u32 s29, s27, 0
	global_load_dwordx2 v[44:45], v162, s[28:29]
	v_cvt_f32_ubyte0_e32 v141, v46
	v_cvt_f32_ubyte1_e32 v143, v46
	v_cvt_f32_ubyte2_e32 v145, v46
	v_cvt_f32_ubyte3_e32 v147, v46
	v_cvt_f32_ubyte0_e32 v149, v47
	v_cvt_f32_ubyte1_e32 v151, v47
	v_cvt_f32_ubyte2_e32 v153, v47
	v_cvt_f32_ubyte3_e32 v155, v47
	s_lshl_b32 s30, s79, 12
	s_add_u32 s28, s26, s30
	s_addc_u32 s29, s27, 0
	global_load_dwordx2 v[46:47], v162, s[28:29]
	v_mul_f32_e32 v186, v124, v108
	v_mul_f32_e32 v187, v125, v108
	v_mul_f32_e32 v188, v140, v108
	v_mul_f32_e32 v189, v141, v108
	v_mul_f32_e32 v156, v126, v109
	v_mul_f32_e32 v157, v127, v109
	v_mul_f32_e32 v158, v142, v109
	v_mul_f32_e32 v159, v143, v109
	v_fmac_f32_e32 v186, v128, v110
	v_fmac_f32_e32 v187, v129, v110
	v_fmac_f32_e32 v188, v144, v110
	v_fmac_f32_e32 v189, v145, v110
	v_fmac_f32_e32 v156, v130, v111
	v_fmac_f32_e32 v157, v131, v111
	v_fmac_f32_e32 v158, v146, v111
	v_fmac_f32_e32 v159, v147, v111
	v_fmac_f32_e32 v186, v132, v112
	v_fmac_f32_e32 v187, v133, v112
	v_fmac_f32_e32 v188, v148, v112
	v_fmac_f32_e32 v189, v149, v112
	v_fmac_f32_e32 v156, v134, v113
	v_fmac_f32_e32 v157, v135, v113
	v_fmac_f32_e32 v158, v150, v113
	v_fmac_f32_e32 v159, v151, v113
	v_fmac_f32_e32 v186, v136, v114
	v_fmac_f32_e32 v187, v137, v114
	v_fmac_f32_e32 v188, v152, v114
	v_fmac_f32_e32 v189, v153, v114
	v_fmac_f32_e32 v156, v138, v115
	v_fmac_f32_e32 v157, v139, v115
	v_fmac_f32_e32 v158, v154, v115
	v_fmac_f32_e32 v159, v155, v115
	v_add_f32_e32 v186, v186, v156
	v_add_f32_e32 v187, v187, v157
	v_add_f32_e32 v188, v188, v158
	v_add_f32_e32 v189, v189, v159
	s_waitcnt vmcnt(29)
	v_cvt_f32_ubyte0_e32 v124, v48
	v_cvt_f32_ubyte1_e32 v126, v48
	v_cvt_f32_ubyte2_e32 v128, v48
	v_cvt_f32_ubyte3_e32 v130, v48
	v_cvt_f32_ubyte0_e32 v132, v49
	v_cvt_f32_ubyte1_e32 v134, v49
	v_cvt_f32_ubyte2_e32 v136, v49
	v_cvt_f32_ubyte3_e32 v138, v49
	s_lshl_b32 s30, s80, 12
	s_add_u32 s28, s26, s30
	s_addc_u32 s29, s27, 0
	global_load_dwordx2 v[48:49], v162, s[28:29]
	v_cvt_f32_ubyte0_e32 v125, v50
	v_cvt_f32_ubyte1_e32 v127, v50
	v_cvt_f32_ubyte2_e32 v129, v50
	v_cvt_f32_ubyte3_e32 v131, v50
	v_cvt_f32_ubyte0_e32 v133, v51
	v_cvt_f32_ubyte1_e32 v135, v51
	v_cvt_f32_ubyte2_e32 v137, v51
	v_cvt_f32_ubyte3_e32 v139, v51
	s_lshl_b32 s30, s81, 12
	s_add_u32 s28, s26, s30
	s_addc_u32 s29, s27, 0
	global_load_dwordx2 v[50:51], v162, s[28:29]
	v_cvt_f32_ubyte0_e32 v140, v52
	v_cvt_f32_ubyte1_e32 v142, v52
	v_cvt_f32_ubyte2_e32 v144, v52
	v_cvt_f32_ubyte3_e32 v146, v52
	v_cvt_f32_ubyte0_e32 v148, v53
	v_cvt_f32_ubyte1_e32 v150, v53
	v_cvt_f32_ubyte2_e32 v152, v53
	v_cvt_f32_ubyte3_e32 v154, v53
	s_lshl_b32 s30, s82, 12
	s_add_u32 s28, s26, s30
	s_addc_u32 s29, s27, 0
	global_load_dwordx2 v[52:53], v162, s[28:29]
	v_cvt_f32_ubyte0_e32 v141, v54
	v_cvt_f32_ubyte1_e32 v143, v54
	v_cvt_f32_ubyte2_e32 v145, v54
	v_cvt_f32_ubyte3_e32 v147, v54
	v_cvt_f32_ubyte0_e32 v149, v55
	v_cvt_f32_ubyte1_e32 v151, v55
	v_cvt_f32_ubyte2_e32 v153, v55
	v_cvt_f32_ubyte3_e32 v155, v55
	s_lshl_b32 s30, s83, 12
	s_add_u32 s28, s26, s30
	s_addc_u32 s29, s27, 0
	global_load_dwordx2 v[54:55], v162, s[28:29]
	v_mul_f32_e32 v190, v124, v108
	v_mul_f32_e32 v191, v125, v108
	v_mul_f32_e32 v192, v140, v108
	v_mul_f32_e32 v193, v141, v108
	v_mul_f32_e32 v156, v126, v109
	v_mul_f32_e32 v157, v127, v109
	v_mul_f32_e32 v158, v142, v109
	v_mul_f32_e32 v159, v143, v109
	v_fmac_f32_e32 v190, v128, v110
	v_fmac_f32_e32 v191, v129, v110
	v_fmac_f32_e32 v192, v144, v110
	v_fmac_f32_e32 v193, v145, v110
	v_fmac_f32_e32 v156, v130, v111
	v_fmac_f32_e32 v157, v131, v111
	v_fmac_f32_e32 v158, v146, v111
	v_fmac_f32_e32 v159, v147, v111
	v_fmac_f32_e32 v190, v132, v112
	v_fmac_f32_e32 v191, v133, v112
	v_fmac_f32_e32 v192, v148, v112
	v_fmac_f32_e32 v193, v149, v112
	v_fmac_f32_e32 v156, v134, v113
	v_fmac_f32_e32 v157, v135, v113
	v_fmac_f32_e32 v158, v150, v113
	v_fmac_f32_e32 v159, v151, v113
	v_fmac_f32_e32 v190, v136, v114
	v_fmac_f32_e32 v191, v137, v114
	v_fmac_f32_e32 v192, v152, v114
	v_fmac_f32_e32 v193, v153, v114
	v_fmac_f32_e32 v156, v138, v115
	v_fmac_f32_e32 v157, v139, v115
	v_fmac_f32_e32 v158, v154, v115
	v_fmac_f32_e32 v159, v155, v115
	v_add_f32_e32 v190, v190, v156
	v_add_f32_e32 v191, v191, v157
	v_add_f32_e32 v192, v192, v158
	v_add_f32_e32 v193, v193, v159
	s_waitcnt vmcnt(29)
	v_cvt_f32_ubyte0_e32 v124, v56
	v_cvt_f32_ubyte1_e32 v126, v56
	v_cvt_f32_ubyte2_e32 v128, v56
	v_cvt_f32_ubyte3_e32 v130, v56
	v_cvt_f32_ubyte0_e32 v132, v57
	v_cvt_f32_ubyte1_e32 v134, v57
	v_cvt_f32_ubyte2_e32 v136, v57
	v_cvt_f32_ubyte3_e32 v138, v57
	s_waitcnt lgkmcnt(0)
	s_load_dwordx16 s[68:83], s[38:39], 0x0 glc
	s_lshl_b32 s30, s84, 12
	s_add_u32 s28, s26, s30
	s_addc_u32 s29, s27, 0
	global_load_dwordx2 v[56:57], v162, s[28:29]
	v_cvt_f32_ubyte0_e32 v125, v58
	v_cvt_f32_ubyte1_e32 v127, v58
	v_cvt_f32_ubyte2_e32 v129, v58
	v_cvt_f32_ubyte3_e32 v131, v58
	v_cvt_f32_ubyte0_e32 v133, v59
	v_cvt_f32_ubyte1_e32 v135, v59
	v_cvt_f32_ubyte2_e32 v137, v59
	v_cvt_f32_ubyte3_e32 v139, v59
	s_lshl_b32 s30, s85, 12
	s_add_u32 s28, s26, s30
	s_addc_u32 s29, s27, 0
	global_load_dwordx2 v[58:59], v162, s[28:29]
	v_cvt_f32_ubyte0_e32 v140, v60
	v_cvt_f32_ubyte1_e32 v142, v60
	v_cvt_f32_ubyte2_e32 v144, v60
	v_cvt_f32_ubyte3_e32 v146, v60
	v_cvt_f32_ubyte0_e32 v148, v61
	v_cvt_f32_ubyte1_e32 v150, v61
	v_cvt_f32_ubyte2_e32 v152, v61
	v_cvt_f32_ubyte3_e32 v154, v61
	s_lshl_b32 s30, s86, 12
	s_add_u32 s28, s26, s30
	s_addc_u32 s29, s27, 0
	global_load_dwordx2 v[60:61], v162, s[28:29]
	v_cvt_f32_ubyte0_e32 v141, v62
	v_cvt_f32_ubyte1_e32 v143, v62
	v_cvt_f32_ubyte2_e32 v145, v62
	v_cvt_f32_ubyte3_e32 v147, v62
	v_cvt_f32_ubyte0_e32 v149, v63
	v_cvt_f32_ubyte1_e32 v151, v63
	v_cvt_f32_ubyte2_e32 v153, v63
	v_cvt_f32_ubyte3_e32 v155, v63
	s_lshl_b32 s30, s87, 12
	s_add_u32 s28, s26, s30
	s_addc_u32 s29, s27, 0
	global_load_dwordx2 v[62:63], v162, s[28:29]
	v_mul_f32_e32 v194, v124, v108
	v_mul_f32_e32 v195, v125, v108
	v_mul_f32_e32 v196, v140, v108
	v_mul_f32_e32 v197, v141, v108
	v_mul_f32_e32 v156, v126, v109
	v_mul_f32_e32 v157, v127, v109
	v_mul_f32_e32 v158, v142, v109
	v_mul_f32_e32 v159, v143, v109
	v_fmac_f32_e32 v194, v128, v110
	v_fmac_f32_e32 v195, v129, v110
	v_fmac_f32_e32 v196, v144, v110
	v_fmac_f32_e32 v197, v145, v110
	v_fmac_f32_e32 v156, v130, v111
	v_fmac_f32_e32 v157, v131, v111
	v_fmac_f32_e32 v158, v146, v111
	v_fmac_f32_e32 v159, v147, v111
	v_fmac_f32_e32 v194, v132, v112
	v_fmac_f32_e32 v195, v133, v112
	v_fmac_f32_e32 v196, v148, v112
	v_fmac_f32_e32 v197, v149, v112
	v_fmac_f32_e32 v156, v134, v113
	v_fmac_f32_e32 v157, v135, v113
	v_fmac_f32_e32 v158, v150, v113
	v_fmac_f32_e32 v159, v151, v113
	v_fmac_f32_e32 v194, v136, v114
	v_fmac_f32_e32 v195, v137, v114
	v_fmac_f32_e32 v196, v152, v114
	v_fmac_f32_e32 v197, v153, v114
	v_fmac_f32_e32 v156, v138, v115
	v_fmac_f32_e32 v157, v139, v115
	v_fmac_f32_e32 v158, v154, v115
	v_fmac_f32_e32 v159, v155, v115
	v_add_f32_e32 v194, v194, v156
	v_add_f32_e32 v195, v195, v157
	v_add_f32_e32 v196, v196, v158
	v_add_f32_e32 v197, v197, v159
	s_waitcnt vmcnt(29)
	v_cvt_f32_ubyte0_e32 v124, v64
	v_cvt_f32_ubyte1_e32 v126, v64
	v_cvt_f32_ubyte2_e32 v128, v64
	v_cvt_f32_ubyte3_e32 v130, v64
	v_cvt_f32_ubyte0_e32 v132, v65
	v_cvt_f32_ubyte1_e32 v134, v65
	v_cvt_f32_ubyte2_e32 v136, v65
	v_cvt_f32_ubyte3_e32 v138, v65
	s_lshl_b32 s30, s88, 12
	s_add_u32 s28, s26, s30
	s_addc_u32 s29, s27, 0
	global_load_dwordx2 v[64:65], v162, s[28:29]
	v_cvt_f32_ubyte0_e32 v125, v66
	v_cvt_f32_ubyte1_e32 v127, v66
	v_cvt_f32_ubyte2_e32 v129, v66
	v_cvt_f32_ubyte3_e32 v131, v66
	v_cvt_f32_ubyte0_e32 v133, v67
	v_cvt_f32_ubyte1_e32 v135, v67
	v_cvt_f32_ubyte2_e32 v137, v67
	v_cvt_f32_ubyte3_e32 v139, v67
	s_lshl_b32 s30, s89, 12
	s_add_u32 s28, s26, s30
	s_addc_u32 s29, s27, 0
	global_load_dwordx2 v[66:67], v162, s[28:29]
	v_cvt_f32_ubyte0_e32 v140, v68
	v_cvt_f32_ubyte1_e32 v142, v68
	v_cvt_f32_ubyte2_e32 v144, v68
	v_cvt_f32_ubyte3_e32 v146, v68
	v_cvt_f32_ubyte0_e32 v148, v69
	v_cvt_f32_ubyte1_e32 v150, v69
	v_cvt_f32_ubyte2_e32 v152, v69
	v_cvt_f32_ubyte3_e32 v154, v69
	s_lshl_b32 s30, s90, 12
	s_add_u32 s28, s26, s30
	s_addc_u32 s29, s27, 0
	global_load_dwordx2 v[68:69], v162, s[28:29]
	v_cvt_f32_ubyte0_e32 v141, v70
	v_cvt_f32_ubyte1_e32 v143, v70
	v_cvt_f32_ubyte2_e32 v145, v70
	v_cvt_f32_ubyte3_e32 v147, v70
	v_cvt_f32_ubyte0_e32 v149, v71
	v_cvt_f32_ubyte1_e32 v151, v71
	v_cvt_f32_ubyte2_e32 v153, v71
	v_cvt_f32_ubyte3_e32 v155, v71
	s_lshl_b32 s30, s91, 12
	s_add_u32 s28, s26, s30
	s_addc_u32 s29, s27, 0
	global_load_dwordx2 v[70:71], v162, s[28:29]
	v_mul_f32_e32 v198, v124, v108
	v_mul_f32_e32 v199, v125, v108
	v_mul_f32_e32 v200, v140, v108
	v_mul_f32_e32 v201, v141, v108
	v_mul_f32_e32 v156, v126, v109
	v_mul_f32_e32 v157, v127, v109
	v_mul_f32_e32 v158, v142, v109
	v_mul_f32_e32 v159, v143, v109
	v_fmac_f32_e32 v198, v128, v110
	v_fmac_f32_e32 v199, v129, v110
	v_fmac_f32_e32 v200, v144, v110
	v_fmac_f32_e32 v201, v145, v110
	v_fmac_f32_e32 v156, v130, v111
	v_fmac_f32_e32 v157, v131, v111
	v_fmac_f32_e32 v158, v146, v111
	v_fmac_f32_e32 v159, v147, v111
	v_fmac_f32_e32 v198, v132, v112
	v_fmac_f32_e32 v199, v133, v112
	v_fmac_f32_e32 v200, v148, v112
	v_fmac_f32_e32 v201, v149, v112
	v_fmac_f32_e32 v156, v134, v113
	v_fmac_f32_e32 v157, v135, v113
	v_fmac_f32_e32 v158, v150, v113
	v_fmac_f32_e32 v159, v151, v113
	v_fmac_f32_e32 v198, v136, v114
	v_fmac_f32_e32 v199, v137, v114
	v_fmac_f32_e32 v200, v152, v114
	v_fmac_f32_e32 v201, v153, v114
	v_fmac_f32_e32 v156, v138, v115
	v_fmac_f32_e32 v157, v139, v115
	v_fmac_f32_e32 v158, v154, v115
	v_fmac_f32_e32 v159, v155, v115
	v_add_f32_e32 v198, v198, v156
	v_add_f32_e32 v199, v199, v157
	v_add_f32_e32 v200, v200, v158
	v_add_f32_e32 v201, v201, v159
	s_waitcnt vmcnt(29)
	v_cvt_f32_ubyte0_e32 v124, v72
	v_cvt_f32_ubyte1_e32 v126, v72
	v_cvt_f32_ubyte2_e32 v128, v72
	v_cvt_f32_ubyte3_e32 v130, v72
	v_cvt_f32_ubyte0_e32 v132, v73
	v_cvt_f32_ubyte1_e32 v134, v73
	v_cvt_f32_ubyte2_e32 v136, v73
	v_cvt_f32_ubyte3_e32 v138, v73
	s_lshl_b32 s30, s92, 12
	s_add_u32 s28, s26, s30
	s_addc_u32 s29, s27, 0
	global_load_dwordx2 v[72:73], v162, s[28:29]
	v_cvt_f32_ubyte0_e32 v125, v74
	v_cvt_f32_ubyte1_e32 v127, v74
	v_cvt_f32_ubyte2_e32 v129, v74
	v_cvt_f32_ubyte3_e32 v131, v74
	v_cvt_f32_ubyte0_e32 v133, v75
	v_cvt_f32_ubyte1_e32 v135, v75
	v_cvt_f32_ubyte2_e32 v137, v75
	v_cvt_f32_ubyte3_e32 v139, v75
	s_lshl_b32 s30, s93, 12
	s_add_u32 s28, s26, s30
	s_addc_u32 s29, s27, 0
	global_load_dwordx2 v[74:75], v162, s[28:29]
	v_cvt_f32_ubyte0_e32 v140, v76
	v_cvt_f32_ubyte1_e32 v142, v76
	v_cvt_f32_ubyte2_e32 v144, v76
	v_cvt_f32_ubyte3_e32 v146, v76
	v_cvt_f32_ubyte0_e32 v148, v77
	v_cvt_f32_ubyte1_e32 v150, v77
	v_cvt_f32_ubyte2_e32 v152, v77
	v_cvt_f32_ubyte3_e32 v154, v77
	s_lshl_b32 s30, s94, 12
	s_add_u32 s28, s26, s30
	s_addc_u32 s29, s27, 0
	global_load_dwordx2 v[76:77], v162, s[28:29]
	v_cvt_f32_ubyte0_e32 v141, v78
	v_cvt_f32_ubyte1_e32 v143, v78
	v_cvt_f32_ubyte2_e32 v145, v78
	v_cvt_f32_ubyte3_e32 v147, v78
	v_cvt_f32_ubyte0_e32 v149, v79
	v_cvt_f32_ubyte1_e32 v151, v79
	v_cvt_f32_ubyte2_e32 v153, v79
	v_cvt_f32_ubyte3_e32 v155, v79
	s_lshl_b32 s30, s95, 12
	s_add_u32 s28, s26, s30
	s_addc_u32 s29, s27, 0
	global_load_dwordx2 v[78:79], v162, s[28:29]
	v_mul_f32_e32 v202, v124, v108
	v_mul_f32_e32 v203, v125, v108
	v_mul_f32_e32 v204, v140, v108
	v_mul_f32_e32 v205, v141, v108
	v_mul_f32_e32 v156, v126, v109
	v_mul_f32_e32 v157, v127, v109
	v_mul_f32_e32 v158, v142, v109
	v_mul_f32_e32 v159, v143, v109
	v_fmac_f32_e32 v202, v128, v110
	v_fmac_f32_e32 v203, v129, v110
	v_fmac_f32_e32 v204, v144, v110
	v_fmac_f32_e32 v205, v145, v110
	v_fmac_f32_e32 v156, v130, v111
	v_fmac_f32_e32 v157, v131, v111
	v_fmac_f32_e32 v158, v146, v111
	v_fmac_f32_e32 v159, v147, v111
	v_fmac_f32_e32 v202, v132, v112
	v_fmac_f32_e32 v203, v133, v112
	v_fmac_f32_e32 v204, v148, v112
	v_fmac_f32_e32 v205, v149, v112
	v_fmac_f32_e32 v156, v134, v113
	v_fmac_f32_e32 v157, v135, v113
	v_fmac_f32_e32 v158, v150, v113
	v_fmac_f32_e32 v159, v151, v113
	v_fmac_f32_e32 v202, v136, v114
	v_fmac_f32_e32 v203, v137, v114
	v_fmac_f32_e32 v204, v152, v114
	v_fmac_f32_e32 v205, v153, v114
	v_fmac_f32_e32 v156, v138, v115
	v_fmac_f32_e32 v157, v139, v115
	v_fmac_f32_e32 v158, v154, v115
	v_fmac_f32_e32 v159, v155, v115
	v_add_f32_e32 v202, v202, v156
	v_add_f32_e32 v203, v203, v157
	v_add_f32_e32 v204, v204, v158
	v_add_f32_e32 v205, v205, v159
	s_waitcnt vmcnt(29)
	v_cvt_f32_ubyte0_e32 v124, v80
	v_cvt_f32_ubyte1_e32 v126, v80
	v_cvt_f32_ubyte2_e32 v128, v80
	v_cvt_f32_ubyte3_e32 v130, v80
	v_cvt_f32_ubyte0_e32 v132, v81
	v_cvt_f32_ubyte1_e32 v134, v81
	v_cvt_f32_ubyte2_e32 v136, v81
	v_cvt_f32_ubyte3_e32 v138, v81
	s_lshl_b32 s30, s96, 12
	s_add_u32 s28, s26, s30
	s_addc_u32 s29, s27, 0
	global_load_dwordx2 v[80:81], v162, s[28:29]
	v_cvt_f32_ubyte0_e32 v125, v82
	v_cvt_f32_ubyte1_e32 v127, v82
	v_cvt_f32_ubyte2_e32 v129, v82
	v_cvt_f32_ubyte3_e32 v131, v82
	v_cvt_f32_ubyte0_e32 v133, v83
	v_cvt_f32_ubyte1_e32 v135, v83
	v_cvt_f32_ubyte2_e32 v137, v83
	v_cvt_f32_ubyte3_e32 v139, v83
	s_lshl_b32 s30, s97, 12
	s_add_u32 s28, s26, s30
	s_addc_u32 s29, s27, 0
	global_load_dwordx2 v[82:83], v162, s[28:29]
	v_cvt_f32_ubyte0_e32 v140, v84
	v_cvt_f32_ubyte1_e32 v142, v84
	v_cvt_f32_ubyte2_e32 v144, v84
	v_cvt_f32_ubyte3_e32 v146, v84
	v_cvt_f32_ubyte0_e32 v148, v85
	v_cvt_f32_ubyte1_e32 v150, v85
	v_cvt_f32_ubyte2_e32 v152, v85
	v_cvt_f32_ubyte3_e32 v154, v85
	s_lshl_b32 s30, s98, 12
	s_add_u32 s28, s26, s30
	s_addc_u32 s29, s27, 0
	global_load_dwordx2 v[84:85], v162, s[28:29]
	v_cvt_f32_ubyte0_e32 v141, v86
	v_cvt_f32_ubyte1_e32 v143, v86
	v_cvt_f32_ubyte2_e32 v145, v86
	v_cvt_f32_ubyte3_e32 v147, v86
	v_cvt_f32_ubyte0_e32 v149, v87
	v_cvt_f32_ubyte1_e32 v151, v87
	v_cvt_f32_ubyte2_e32 v153, v87
	v_cvt_f32_ubyte3_e32 v155, v87
	s_lshl_b32 s30, s99, 12
	s_add_u32 s28, s26, s30
	s_addc_u32 s29, s27, 0
	global_load_dwordx2 v[86:87], v162, s[28:29]
	v_mul_f32_e32 v206, v124, v108
	v_mul_f32_e32 v207, v125, v108
	v_mul_f32_e32 v208, v140, v108
	v_mul_f32_e32 v209, v141, v108
	v_mul_f32_e32 v156, v126, v109
	v_mul_f32_e32 v157, v127, v109
	v_mul_f32_e32 v158, v142, v109
	v_mul_f32_e32 v159, v143, v109
	v_fmac_f32_e32 v206, v128, v110
	v_fmac_f32_e32 v207, v129, v110
	v_fmac_f32_e32 v208, v144, v110
	v_fmac_f32_e32 v209, v145, v110
	v_fmac_f32_e32 v156, v130, v111
	v_fmac_f32_e32 v157, v131, v111
	v_fmac_f32_e32 v158, v146, v111
	v_fmac_f32_e32 v159, v147, v111
	v_fmac_f32_e32 v206, v132, v112
	v_fmac_f32_e32 v207, v133, v112
	v_fmac_f32_e32 v208, v148, v112
	v_fmac_f32_e32 v209, v149, v112
	v_fmac_f32_e32 v156, v134, v113
	v_fmac_f32_e32 v157, v135, v113
	v_fmac_f32_e32 v158, v150, v113
	v_fmac_f32_e32 v159, v151, v113
	v_fmac_f32_e32 v206, v136, v114
	v_fmac_f32_e32 v207, v137, v114
	v_fmac_f32_e32 v208, v152, v114
	v_fmac_f32_e32 v209, v153, v114
	v_fmac_f32_e32 v156, v138, v115
	v_fmac_f32_e32 v157, v139, v115
	v_fmac_f32_e32 v158, v154, v115
	v_fmac_f32_e32 v159, v155, v115
	v_add_f32_e32 v206, v206, v156
	v_add_f32_e32 v207, v207, v157
	v_add_f32_e32 v208, v208, v158
	v_add_f32_e32 v209, v209, v159
	v_permlane32_swap_b32_e32 v178, v194
	v_permlane32_swap_b32_e32 v179, v195
	v_permlane32_swap_b32_e32 v180, v196
	v_permlane32_swap_b32_e32 v181, v197
	v_permlane32_swap_b32_e32 v182, v198
	v_permlane32_swap_b32_e32 v183, v199
	v_permlane32_swap_b32_e32 v184, v200
	v_permlane32_swap_b32_e32 v185, v201
	v_permlane32_swap_b32_e32 v186, v202
	v_permlane32_swap_b32_e32 v187, v203
	v_permlane32_swap_b32_e32 v188, v204
	v_permlane32_swap_b32_e32 v189, v205
	v_permlane32_swap_b32_e32 v190, v206
	v_permlane32_swap_b32_e32 v191, v207
	v_permlane32_swap_b32_e32 v192, v208
	v_permlane32_swap_b32_e32 v193, v209
	v_add_f32_e32 v178, v178, v194
	v_add_f32_e32 v179, v179, v195
	v_add_f32_e32 v180, v180, v196
	v_add_f32_e32 v181, v181, v197
	v_add_f32_e32 v182, v182, v198
	v_add_f32_e32 v183, v183, v199
	v_add_f32_e32 v184, v184, v200
	v_add_f32_e32 v185, v185, v201
	v_add_f32_e32 v186, v186, v202
	v_add_f32_e32 v187, v187, v203
	v_add_f32_e32 v188, v188, v204
	v_add_f32_e32 v189, v189, v205
	v_add_f32_e32 v190, v190, v206
	v_add_f32_e32 v191, v191, v207
	v_add_f32_e32 v192, v192, v208
	v_add_f32_e32 v193, v193, v209
	v_permlane16_swap_b32_e32 v178, v186
	v_permlane16_swap_b32_e32 v179, v187
	v_permlane16_swap_b32_e32 v180, v188
	v_permlane16_swap_b32_e32 v181, v189
	v_permlane16_swap_b32_e32 v182, v190
	v_permlane16_swap_b32_e32 v183, v191
	v_permlane16_swap_b32_e32 v184, v192
	v_permlane16_swap_b32_e32 v185, v193
	v_add_f32_e32 v178, v178, v186
	v_add_f32_e32 v179, v179, v187
	v_add_f32_e32 v180, v180, v188
	v_add_f32_e32 v181, v181, v189
	v_add_f32_e32 v182, v182, v190
	v_add_f32_e32 v183, v183, v191
	v_add_f32_e32 v184, v184, v192
	v_add_f32_e32 v185, v185, v193
	v_cndmask_b32_e64 v2, v178, v182, s[8:9]
	v_cndmask_b32_e64 v3, v179, v183, s[8:9]
	v_cndmask_b32_e64 v4, v180, v184, s[8:9]
	v_cndmask_b32_e64 v5, v181, v185, s[8:9]
	v_cndmask_b32_e64 v6, v182, v178, s[8:9]
	v_cndmask_b32_e64 v7, v183, v179, s[8:9]
	v_cndmask_b32_e64 v8, v184, v180, s[8:9]
	v_cndmask_b32_e64 v9, v185, v181, s[8:9]
	v_add_f32_dpp v6, v2, v6 row_ror:8 row_mask:0xf bank_mask:0xf
	v_add_f32_dpp v7, v3, v7 row_ror:8 row_mask:0xf bank_mask:0xf
	v_add_f32_dpp v8, v4, v8 row_ror:8 row_mask:0xf bank_mask:0xf
	v_add_f32_dpp v9, v5, v9 row_ror:8 row_mask:0xf bank_mask:0xf
	v_cndmask_b32_e64 v2, v6, v8, s[10:11]
	v_cndmask_b32_e64 v3, v7, v9, s[10:11]
	v_cndmask_b32_e64 v4, v8, v6, s[10:11]
	v_cndmask_b32_e64 v5, v9, v7, s[10:11]
	v_add_f32_dpp v4, v2, v4 row_half_mirror row_mask:0xf bank_mask:0xf
	v_add_f32_dpp v5, v3, v5 row_half_mirror row_mask:0xf bank_mask:0xf
	v_cndmask_b32_e64 v2, v4, v5, s[14:15]
	v_cndmask_b32_e64 v3, v5, v4, s[14:15]
	s_nop 0
	v_add_f32_dpp v3, v2, v3 quad_perm:[2,3,0,1] row_mask:0xf bank_mask:0xf
	s_nop 1
	v_add_f32_dpp v11, v3, v3 quad_perm:[1,0,3,2] row_mask:0xf bank_mask:0xf
	s_mov_b64 exec, s[2:3]
	global_store_dword v[22:23], v11, off offset:256
	s_mov_b64 exec, -1
	s_waitcnt vmcnt(29)
	v_cvt_f32_ubyte0_e32 v124, v24
	v_cvt_f32_ubyte1_e32 v126, v24
	v_cvt_f32_ubyte2_e32 v128, v24
	v_cvt_f32_ubyte3_e32 v130, v24
	v_cvt_f32_ubyte0_e32 v132, v25
	v_cvt_f32_ubyte1_e32 v134, v25
	v_cvt_f32_ubyte2_e32 v136, v25
	v_cvt_f32_ubyte3_e32 v138, v25
	v_cvt_f32_ubyte0_e32 v125, v26
	v_cvt_f32_ubyte1_e32 v127, v26
	v_cvt_f32_ubyte2_e32 v129, v26
	v_cvt_f32_ubyte3_e32 v131, v26
	v_cvt_f32_ubyte0_e32 v133, v27
	v_cvt_f32_ubyte1_e32 v135, v27
	v_cvt_f32_ubyte2_e32 v137, v27
	v_cvt_f32_ubyte3_e32 v139, v27
	v_cvt_f32_ubyte0_e32 v140, v28
	v_cvt_f32_ubyte1_e32 v142, v28
	v_cvt_f32_ubyte2_e32 v144, v28
	v_cvt_f32_ubyte3_e32 v146, v28
	v_cvt_f32_ubyte0_e32 v148, v29
	v_cvt_f32_ubyte1_e32 v150, v29
	v_cvt_f32_ubyte2_e32 v152, v29
	v_cvt_f32_ubyte3_e32 v154, v29
	v_cvt_f32_ubyte0_e32 v141, v30
	v_cvt_f32_ubyte1_e32 v143, v30
	v_cvt_f32_ubyte2_e32 v145, v30
	v_cvt_f32_ubyte3_e32 v147, v30
	v_cvt_f32_ubyte0_e32 v149, v31
	v_cvt_f32_ubyte1_e32 v151, v31
	v_cvt_f32_ubyte2_e32 v153, v31
	v_cvt_f32_ubyte3_e32 v155, v31
	v_mul_f32_e32 v178, v124, v108
	v_mul_f32_e32 v179, v125, v108
	v_mul_f32_e32 v180, v140, v108
	v_mul_f32_e32 v181, v141, v108
	v_mul_f32_e32 v156, v126, v109
	v_mul_f32_e32 v157, v127, v109
	v_mul_f32_e32 v158, v142, v109
	v_mul_f32_e32 v159, v143, v109
	v_fmac_f32_e32 v178, v128, v110
	v_fmac_f32_e32 v179, v129, v110
	v_fmac_f32_e32 v180, v144, v110
	v_fmac_f32_e32 v181, v145, v110
	v_fmac_f32_e32 v156, v130, v111
	v_fmac_f32_e32 v157, v131, v111
	v_fmac_f32_e32 v158, v146, v111
	v_fmac_f32_e32 v159, v147, v111
	v_fmac_f32_e32 v178, v132, v112
	v_fmac_f32_e32 v179, v133, v112
	v_fmac_f32_e32 v180, v148, v112
	v_fmac_f32_e32 v181, v149, v112
	v_fmac_f32_e32 v156, v134, v113
	v_fmac_f32_e32 v157, v135, v113
	v_fmac_f32_e32 v158, v150, v113
	v_fmac_f32_e32 v159, v151, v113
	v_fmac_f32_e32 v178, v136, v114
	v_fmac_f32_e32 v179, v137, v114
	v_fmac_f32_e32 v180, v152, v114
	v_fmac_f32_e32 v181, v153, v114
	v_fmac_f32_e32 v156, v138, v115
	v_fmac_f32_e32 v157, v139, v115
	v_fmac_f32_e32 v158, v154, v115
	v_fmac_f32_e32 v159, v155, v115
	v_add_f32_e32 v178, v178, v156
	v_add_f32_e32 v179, v179, v157
	v_add_f32_e32 v180, v180, v158
	v_add_f32_e32 v181, v181, v159
	s_waitcnt vmcnt(25)
	v_cvt_f32_ubyte0_e32 v124, v32
	v_cvt_f32_ubyte1_e32 v126, v32
	v_cvt_f32_ubyte2_e32 v128, v32
	v_cvt_f32_ubyte3_e32 v130, v32
	v_cvt_f32_ubyte0_e32 v132, v33
	v_cvt_f32_ubyte1_e32 v134, v33
	v_cvt_f32_ubyte2_e32 v136, v33
	v_cvt_f32_ubyte3_e32 v138, v33
	v_cvt_f32_ubyte0_e32 v125, v34
	v_cvt_f32_ubyte1_e32 v127, v34
	v_cvt_f32_ubyte2_e32 v129, v34
	v_cvt_f32_ubyte3_e32 v131, v34
	v_cvt_f32_ubyte0_e32 v133, v35
	v_cvt_f32_ubyte1_e32 v135, v35
	v_cvt_f32_ubyte2_e32 v137, v35
	v_cvt_f32_ubyte3_e32 v139, v35
	v_cvt_f32_ubyte0_e32 v140, v36
	v_cvt_f32_ubyte1_e32 v142, v36
	v_cvt_f32_ubyte2_e32 v144, v36
	v_cvt_f32_ubyte3_e32 v146, v36
	v_cvt_f32_ubyte0_e32 v148, v37
	v_cvt_f32_ubyte1_e32 v150, v37
	v_cvt_f32_ubyte2_e32 v152, v37
	v_cvt_f32_ubyte3_e32 v154, v37
	v_cvt_f32_ubyte0_e32 v141, v38
	v_cvt_f32_ubyte1_e32 v143, v38
	v_cvt_f32_ubyte2_e32 v145, v38
	v_cvt_f32_ubyte3_e32 v147, v38
	v_cvt_f32_ubyte0_e32 v149, v39
	v_cvt_f32_ubyte1_e32 v151, v39
	v_cvt_f32_ubyte2_e32 v153, v39
	v_cvt_f32_ubyte3_e32 v155, v39
	v_mul_f32_e32 v182, v124, v108
	v_mul_f32_e32 v183, v125, v108
	v_mul_f32_e32 v184, v140, v108
	v_mul_f32_e32 v185, v141, v108
	v_mul_f32_e32 v156, v126, v109
	v_mul_f32_e32 v157, v127, v109
	v_mul_f32_e32 v158, v142, v109
	v_mul_f32_e32 v159, v143, v109
	v_fmac_f32_e32 v182, v128, v110
	v_fmac_f32_e32 v183, v129, v110
	v_fmac_f32_e32 v184, v144, v110
	v_fmac_f32_e32 v185, v145, v110
	v_fmac_f32_e32 v156, v130, v111
	v_fmac_f32_e32 v157, v131, v111
	v_fmac_f32_e32 v158, v146, v111
	v_fmac_f32_e32 v159, v147, v111
	v_fmac_f32_e32 v182, v132, v112
	v_fmac_f32_e32 v183, v133, v112
	v_fmac_f32_e32 v184, v148, v112
	v_fmac_f32_e32 v185, v149, v112
	v_fmac_f32_e32 v156, v134, v113
	v_fmac_f32_e32 v157, v135, v113
	v_fmac_f32_e32 v158, v150, v113
	v_fmac_f32_e32 v159, v151, v113
	v_fmac_f32_e32 v182, v136, v114
	v_fmac_f32_e32 v183, v137, v114
	v_fmac_f32_e32 v184, v152, v114
	v_fmac_f32_e32 v185, v153, v114
	v_fmac_f32_e32 v156, v138, v115
	v_fmac_f32_e32 v157, v139, v115
	v_fmac_f32_e32 v158, v154, v115
	v_fmac_f32_e32 v159, v155, v115
	v_add_f32_e32 v182, v182, v156
	v_add_f32_e32 v183, v183, v157
	v_add_f32_e32 v184, v184, v158
	v_add_f32_e32 v185, v185, v159
	s_waitcnt vmcnt(21)
	v_cvt_f32_ubyte0_e32 v124, v40
	v_cvt_f32_ubyte1_e32 v126, v40
	v_cvt_f32_ubyte2_e32 v128, v40
	v_cvt_f32_ubyte3_e32 v130, v40
	v_cvt_f32_ubyte0_e32 v132, v41
	v_cvt_f32_ubyte1_e32 v134, v41
	v_cvt_f32_ubyte2_e32 v136, v41
	v_cvt_f32_ubyte3_e32 v138, v41
	v_cvt_f32_ubyte0_e32 v125, v42
	v_cvt_f32_ubyte1_e32 v127, v42
	v_cvt_f32_ubyte2_e32 v129, v42
	v_cvt_f32_ubyte3_e32 v131, v42
	v_cvt_f32_ubyte0_e32 v133, v43
	v_cvt_f32_ubyte1_e32 v135, v43
	v_cvt_f32_ubyte2_e32 v137, v43
	v_cvt_f32_ubyte3_e32 v139, v43
	v_cvt_f32_ubyte0_e32 v140, v44
	v_cvt_f32_ubyte1_e32 v142, v44
	v_cvt_f32_ubyte2_e32 v144, v44
	v_cvt_f32_ubyte3_e32 v146, v44
	v_cvt_f32_ubyte0_e32 v148, v45
	v_cvt_f32_ubyte1_e32 v150, v45
	v_cvt_f32_ubyte2_e32 v152, v45
	v_cvt_f32_ubyte3_e32 v154, v45
	v_cvt_f32_ubyte0_e32 v141, v46
	v_cvt_f32_ubyte1_e32 v143, v46
	v_cvt_f32_ubyte2_e32 v145, v46
	v_cvt_f32_ubyte3_e32 v147, v46
	v_cvt_f32_ubyte0_e32 v149, v47
	v_cvt_f32_ubyte1_e32 v151, v47
	v_cvt_f32_ubyte2_e32 v153, v47
	v_cvt_f32_ubyte3_e32 v155, v47
	v_mul_f32_e32 v186, v124, v108
	v_mul_f32_e32 v187, v125, v108
	v_mul_f32_e32 v188, v140, v108
	v_mul_f32_e32 v189, v141, v108
	v_mul_f32_e32 v156, v126, v109
	v_mul_f32_e32 v157, v127, v109
	v_mul_f32_e32 v158, v142, v109
	v_mul_f32_e32 v159, v143, v109
	v_fmac_f32_e32 v186, v128, v110
	v_fmac_f32_e32 v187, v129, v110
	v_fmac_f32_e32 v188, v144, v110
	v_fmac_f32_e32 v189, v145, v110
	v_fmac_f32_e32 v156, v130, v111
	v_fmac_f32_e32 v157, v131, v111
	v_fmac_f32_e32 v158, v146, v111
	v_fmac_f32_e32 v159, v147, v111
	v_fmac_f32_e32 v186, v132, v112
	v_fmac_f32_e32 v187, v133, v112
	v_fmac_f32_e32 v188, v148, v112
	v_fmac_f32_e32 v189, v149, v112
	v_fmac_f32_e32 v156, v134, v113
	v_fmac_f32_e32 v157, v135, v113
	v_fmac_f32_e32 v158, v150, v113
	v_fmac_f32_e32 v159, v151, v113
	v_fmac_f32_e32 v186, v136, v114
	v_fmac_f32_e32 v187, v137, v114
	v_fmac_f32_e32 v188, v152, v114
	v_fmac_f32_e32 v189, v153, v114
	v_fmac_f32_e32 v156, v138, v115
	v_fmac_f32_e32 v157, v139, v115
	v_fmac_f32_e32 v158, v154, v115
	v_fmac_f32_e32 v159, v155, v115
	v_add_f32_e32 v186, v186, v156
	v_add_f32_e32 v187, v187, v157
	v_add_f32_e32 v188, v188, v158
	v_add_f32_e32 v189, v189, v159
	s_waitcnt vmcnt(17)
	v_cvt_f32_ubyte0_e32 v124, v48
	v_cvt_f32_ubyte1_e32 v126, v48
	v_cvt_f32_ubyte2_e32 v128, v48
	v_cvt_f32_ubyte3_e32 v130, v48
	v_cvt_f32_ubyte0_e32 v132, v49
	v_cvt_f32_ubyte1_e32 v134, v49
	v_cvt_f32_ubyte2_e32 v136, v49
	v_cvt_f32_ubyte3_e32 v138, v49
	v_cvt_f32_ubyte0_e32 v125, v50
	v_cvt_f32_ubyte1_e32 v127, v50
	v_cvt_f32_ubyte2_e32 v129, v50
	v_cvt_f32_ubyte3_e32 v131, v50
	v_cvt_f32_ubyte0_e32 v133, v51
	v_cvt_f32_ubyte1_e32 v135, v51
	v_cvt_f32_ubyte2_e32 v137, v51
	v_cvt_f32_ubyte3_e32 v139, v51
	v_cvt_f32_ubyte0_e32 v140, v52
	v_cvt_f32_ubyte1_e32 v142, v52
	v_cvt_f32_ubyte2_e32 v144, v52
	v_cvt_f32_ubyte3_e32 v146, v52
	v_cvt_f32_ubyte0_e32 v148, v53
	v_cvt_f32_ubyte1_e32 v150, v53
	v_cvt_f32_ubyte2_e32 v152, v53
	v_cvt_f32_ubyte3_e32 v154, v53
	v_cvt_f32_ubyte0_e32 v141, v54
	v_cvt_f32_ubyte1_e32 v143, v54
	v_cvt_f32_ubyte2_e32 v145, v54
	v_cvt_f32_ubyte3_e32 v147, v54
	v_cvt_f32_ubyte0_e32 v149, v55
	v_cvt_f32_ubyte1_e32 v151, v55
	v_cvt_f32_ubyte2_e32 v153, v55
	v_cvt_f32_ubyte3_e32 v155, v55
	v_mul_f32_e32 v190, v124, v108
	v_mul_f32_e32 v191, v125, v108
	v_mul_f32_e32 v192, v140, v108
	v_mul_f32_e32 v193, v141, v108
	v_mul_f32_e32 v156, v126, v109
	v_mul_f32_e32 v157, v127, v109
	v_mul_f32_e32 v158, v142, v109
	v_mul_f32_e32 v159, v143, v109
	v_fmac_f32_e32 v190, v128, v110
	v_fmac_f32_e32 v191, v129, v110
	v_fmac_f32_e32 v192, v144, v110
	v_fmac_f32_e32 v193, v145, v110
	v_fmac_f32_e32 v156, v130, v111
	v_fmac_f32_e32 v157, v131, v111
	v_fmac_f32_e32 v158, v146, v111
	v_fmac_f32_e32 v159, v147, v111
	v_fmac_f32_e32 v190, v132, v112
	v_fmac_f32_e32 v191, v133, v112
	v_fmac_f32_e32 v192, v148, v112
	v_fmac_f32_e32 v193, v149, v112
	v_fmac_f32_e32 v156, v134, v113
	v_fmac_f32_e32 v157, v135, v113
	v_fmac_f32_e32 v158, v150, v113
	v_fmac_f32_e32 v159, v151, v113
	v_fmac_f32_e32 v190, v136, v114
	v_fmac_f32_e32 v191, v137, v114
	v_fmac_f32_e32 v192, v152, v114
	v_fmac_f32_e32 v193, v153, v114
	v_fmac_f32_e32 v156, v138, v115
	v_fmac_f32_e32 v157, v139, v115
	v_fmac_f32_e32 v158, v154, v115
	v_fmac_f32_e32 v159, v155, v115
	v_add_f32_e32 v190, v190, v156
	v_add_f32_e32 v191, v191, v157
	v_add_f32_e32 v192, v192, v158
	v_add_f32_e32 v193, v193, v159
	s_waitcnt vmcnt(13)
	v_cvt_f32_ubyte0_e32 v124, v56
	v_cvt_f32_ubyte1_e32 v126, v56
	v_cvt_f32_ubyte2_e32 v128, v56
	v_cvt_f32_ubyte3_e32 v130, v56
	v_cvt_f32_ubyte0_e32 v132, v57
	v_cvt_f32_ubyte1_e32 v134, v57
	v_cvt_f32_ubyte2_e32 v136, v57
	v_cvt_f32_ubyte3_e32 v138, v57
	v_cvt_f32_ubyte0_e32 v125, v58
	v_cvt_f32_ubyte1_e32 v127, v58
	v_cvt_f32_ubyte2_e32 v129, v58
	v_cvt_f32_ubyte3_e32 v131, v58
	v_cvt_f32_ubyte0_e32 v133, v59
	v_cvt_f32_ubyte1_e32 v135, v59
	v_cvt_f32_ubyte2_e32 v137, v59
	v_cvt_f32_ubyte3_e32 v139, v59
	v_cvt_f32_ubyte0_e32 v140, v60
	v_cvt_f32_ubyte1_e32 v142, v60
	v_cvt_f32_ubyte2_e32 v144, v60
	v_cvt_f32_ubyte3_e32 v146, v60
	v_cvt_f32_ubyte0_e32 v148, v61
	v_cvt_f32_ubyte1_e32 v150, v61
	v_cvt_f32_ubyte2_e32 v152, v61
	v_cvt_f32_ubyte3_e32 v154, v61
	v_cvt_f32_ubyte0_e32 v141, v62
	v_cvt_f32_ubyte1_e32 v143, v62
	v_cvt_f32_ubyte2_e32 v145, v62
	v_cvt_f32_ubyte3_e32 v147, v62
	v_cvt_f32_ubyte0_e32 v149, v63
	v_cvt_f32_ubyte1_e32 v151, v63
	v_cvt_f32_ubyte2_e32 v153, v63
	v_cvt_f32_ubyte3_e32 v155, v63
	v_mul_f32_e32 v194, v124, v108
	v_mul_f32_e32 v195, v125, v108
	v_mul_f32_e32 v196, v140, v108
	v_mul_f32_e32 v197, v141, v108
	v_mul_f32_e32 v156, v126, v109
	v_mul_f32_e32 v157, v127, v109
	v_mul_f32_e32 v158, v142, v109
	v_mul_f32_e32 v159, v143, v109
	v_fmac_f32_e32 v194, v128, v110
	v_fmac_f32_e32 v195, v129, v110
	v_fmac_f32_e32 v196, v144, v110
	v_fmac_f32_e32 v197, v145, v110
	v_fmac_f32_e32 v156, v130, v111
	v_fmac_f32_e32 v157, v131, v111
	v_fmac_f32_e32 v158, v146, v111
	v_fmac_f32_e32 v159, v147, v111
	v_fmac_f32_e32 v194, v132, v112
	v_fmac_f32_e32 v195, v133, v112
	v_fmac_f32_e32 v196, v148, v112
	v_fmac_f32_e32 v197, v149, v112
	v_fmac_f32_e32 v156, v134, v113
	v_fmac_f32_e32 v157, v135, v113
	v_fmac_f32_e32 v158, v150, v113
	v_fmac_f32_e32 v159, v151, v113
	v_fmac_f32_e32 v194, v136, v114
	v_fmac_f32_e32 v195, v137, v114
	v_fmac_f32_e32 v196, v152, v114
	v_fmac_f32_e32 v197, v153, v114
	v_fmac_f32_e32 v156, v138, v115
	v_fmac_f32_e32 v157, v139, v115
	v_fmac_f32_e32 v158, v154, v115
	v_fmac_f32_e32 v159, v155, v115
	v_add_f32_e32 v194, v194, v156
	v_add_f32_e32 v195, v195, v157
	v_add_f32_e32 v196, v196, v158
	v_add_f32_e32 v197, v197, v159
	s_waitcnt vmcnt(9)
	v_cvt_f32_ubyte0_e32 v124, v64
	v_cvt_f32_ubyte1_e32 v126, v64
	v_cvt_f32_ubyte2_e32 v128, v64
	v_cvt_f32_ubyte3_e32 v130, v64
	v_cvt_f32_ubyte0_e32 v132, v65
	v_cvt_f32_ubyte1_e32 v134, v65
	v_cvt_f32_ubyte2_e32 v136, v65
	v_cvt_f32_ubyte3_e32 v138, v65
	v_cvt_f32_ubyte0_e32 v125, v66
	v_cvt_f32_ubyte1_e32 v127, v66
	v_cvt_f32_ubyte2_e32 v129, v66
	v_cvt_f32_ubyte3_e32 v131, v66
	v_cvt_f32_ubyte0_e32 v133, v67
	v_cvt_f32_ubyte1_e32 v135, v67
	v_cvt_f32_ubyte2_e32 v137, v67
	v_cvt_f32_ubyte3_e32 v139, v67
	v_cvt_f32_ubyte0_e32 v140, v68
	v_cvt_f32_ubyte1_e32 v142, v68
	v_cvt_f32_ubyte2_e32 v144, v68
	v_cvt_f32_ubyte3_e32 v146, v68
	v_cvt_f32_ubyte0_e32 v148, v69
	v_cvt_f32_ubyte1_e32 v150, v69
	v_cvt_f32_ubyte2_e32 v152, v69
	v_cvt_f32_ubyte3_e32 v154, v69
	v_cvt_f32_ubyte0_e32 v141, v70
	v_cvt_f32_ubyte1_e32 v143, v70
	v_cvt_f32_ubyte2_e32 v145, v70
	v_cvt_f32_ubyte3_e32 v147, v70
	v_cvt_f32_ubyte0_e32 v149, v71
	v_cvt_f32_ubyte1_e32 v151, v71
	v_cvt_f32_ubyte2_e32 v153, v71
	v_cvt_f32_ubyte3_e32 v155, v71
	v_mul_f32_e32 v198, v124, v108
	v_mul_f32_e32 v199, v125, v108
	v_mul_f32_e32 v200, v140, v108
	v_mul_f32_e32 v201, v141, v108
	v_mul_f32_e32 v156, v126, v109
	v_mul_f32_e32 v157, v127, v109
	v_mul_f32_e32 v158, v142, v109
	v_mul_f32_e32 v159, v143, v109
	v_fmac_f32_e32 v198, v128, v110
	v_fmac_f32_e32 v199, v129, v110
	v_fmac_f32_e32 v200, v144, v110
	v_fmac_f32_e32 v201, v145, v110
	v_fmac_f32_e32 v156, v130, v111
	v_fmac_f32_e32 v157, v131, v111
	v_fmac_f32_e32 v158, v146, v111
	v_fmac_f32_e32 v159, v147, v111
	v_fmac_f32_e32 v198, v132, v112
	v_fmac_f32_e32 v199, v133, v112
	v_fmac_f32_e32 v200, v148, v112
	v_fmac_f32_e32 v201, v149, v112
	v_fmac_f32_e32 v156, v134, v113
	v_fmac_f32_e32 v157, v135, v113
	v_fmac_f32_e32 v158, v150, v113
	v_fmac_f32_e32 v159, v151, v113
	v_fmac_f32_e32 v198, v136, v114
	v_fmac_f32_e32 v199, v137, v114
	v_fmac_f32_e32 v200, v152, v114
	v_fmac_f32_e32 v201, v153, v114
	v_fmac_f32_e32 v156, v138, v115
	v_fmac_f32_e32 v157, v139, v115
	v_fmac_f32_e32 v158, v154, v115
	v_fmac_f32_e32 v159, v155, v115
	v_add_f32_e32 v198, v198, v156
	v_add_f32_e32 v199, v199, v157
	v_add_f32_e32 v200, v200, v158
	v_add_f32_e32 v201, v201, v159
	s_waitcnt vmcnt(5)
	v_cvt_f32_ubyte0_e32 v124, v72
	v_cvt_f32_ubyte1_e32 v126, v72
	v_cvt_f32_ubyte2_e32 v128, v72
	v_cvt_f32_ubyte3_e32 v130, v72
	v_cvt_f32_ubyte0_e32 v132, v73
	v_cvt_f32_ubyte1_e32 v134, v73
	v_cvt_f32_ubyte2_e32 v136, v73
	v_cvt_f32_ubyte3_e32 v138, v73
	v_cvt_f32_ubyte0_e32 v125, v74
	v_cvt_f32_ubyte1_e32 v127, v74
	v_cvt_f32_ubyte2_e32 v129, v74
	v_cvt_f32_ubyte3_e32 v131, v74
	v_cvt_f32_ubyte0_e32 v133, v75
	v_cvt_f32_ubyte1_e32 v135, v75
	v_cvt_f32_ubyte2_e32 v137, v75
	v_cvt_f32_ubyte3_e32 v139, v75
	v_cvt_f32_ubyte0_e32 v140, v76
	v_cvt_f32_ubyte1_e32 v142, v76
	v_cvt_f32_ubyte2_e32 v144, v76
	v_cvt_f32_ubyte3_e32 v146, v76
	v_cvt_f32_ubyte0_e32 v148, v77
	v_cvt_f32_ubyte1_e32 v150, v77
	v_cvt_f32_ubyte2_e32 v152, v77
	v_cvt_f32_ubyte3_e32 v154, v77
	v_cvt_f32_ubyte0_e32 v141, v78
	v_cvt_f32_ubyte1_e32 v143, v78
	v_cvt_f32_ubyte2_e32 v145, v78
	v_cvt_f32_ubyte3_e32 v147, v78
	v_cvt_f32_ubyte0_e32 v149, v79
	v_cvt_f32_ubyte1_e32 v151, v79
	v_cvt_f32_ubyte2_e32 v153, v79
	v_cvt_f32_ubyte3_e32 v155, v79
	v_mul_f32_e32 v202, v124, v108
	v_mul_f32_e32 v203, v125, v108
	v_mul_f32_e32 v204, v140, v108
	v_mul_f32_e32 v205, v141, v108
	v_mul_f32_e32 v156, v126, v109
	v_mul_f32_e32 v157, v127, v109
	v_mul_f32_e32 v158, v142, v109
	v_mul_f32_e32 v159, v143, v109
	v_fmac_f32_e32 v202, v128, v110
	v_fmac_f32_e32 v203, v129, v110
	v_fmac_f32_e32 v204, v144, v110
	v_fmac_f32_e32 v205, v145, v110
	v_fmac_f32_e32 v156, v130, v111
	v_fmac_f32_e32 v157, v131, v111
	v_fmac_f32_e32 v158, v146, v111
	v_fmac_f32_e32 v159, v147, v111
	v_fmac_f32_e32 v202, v132, v112
	v_fmac_f32_e32 v203, v133, v112
	v_fmac_f32_e32 v204, v148, v112
	v_fmac_f32_e32 v205, v149, v112
	v_fmac_f32_e32 v156, v134, v113
	v_fmac_f32_e32 v157, v135, v113
	v_fmac_f32_e32 v158, v150, v113
	v_fmac_f32_e32 v159, v151, v113
	v_fmac_f32_e32 v202, v136, v114
	v_fmac_f32_e32 v203, v137, v114
	v_fmac_f32_e32 v204, v152, v114
	v_fmac_f32_e32 v205, v153, v114
	v_fmac_f32_e32 v156, v138, v115
	v_fmac_f32_e32 v157, v139, v115
	v_fmac_f32_e32 v158, v154, v115
	v_fmac_f32_e32 v159, v155, v115
	v_add_f32_e32 v202, v202, v156
	v_add_f32_e32 v203, v203, v157
	v_add_f32_e32 v204, v204, v158
	v_add_f32_e32 v205, v205, v159
	s_waitcnt vmcnt(1)
	v_cvt_f32_ubyte0_e32 v124, v80
	v_cvt_f32_ubyte1_e32 v126, v80
	v_cvt_f32_ubyte2_e32 v128, v80
	v_cvt_f32_ubyte3_e32 v130, v80
	v_cvt_f32_ubyte0_e32 v132, v81
	v_cvt_f32_ubyte1_e32 v134, v81
	v_cvt_f32_ubyte2_e32 v136, v81
	v_cvt_f32_ubyte3_e32 v138, v81
	v_cvt_f32_ubyte0_e32 v125, v82
	v_cvt_f32_ubyte1_e32 v127, v82
	v_cvt_f32_ubyte2_e32 v129, v82
	v_cvt_f32_ubyte3_e32 v131, v82
	v_cvt_f32_ubyte0_e32 v133, v83
	v_cvt_f32_ubyte1_e32 v135, v83
	v_cvt_f32_ubyte2_e32 v137, v83
	v_cvt_f32_ubyte3_e32 v139, v83
	v_cvt_f32_ubyte0_e32 v140, v84
	v_cvt_f32_ubyte1_e32 v142, v84
	v_cvt_f32_ubyte2_e32 v144, v84
	v_cvt_f32_ubyte3_e32 v146, v84
	v_cvt_f32_ubyte0_e32 v148, v85
	v_cvt_f32_ubyte1_e32 v150, v85
	v_cvt_f32_ubyte2_e32 v152, v85
	v_cvt_f32_ubyte3_e32 v154, v85
	v_cvt_f32_ubyte0_e32 v141, v86
	v_cvt_f32_ubyte1_e32 v143, v86
	v_cvt_f32_ubyte2_e32 v145, v86
	v_cvt_f32_ubyte3_e32 v147, v86
	v_cvt_f32_ubyte0_e32 v149, v87
	v_cvt_f32_ubyte1_e32 v151, v87
	v_cvt_f32_ubyte2_e32 v153, v87
	v_cvt_f32_ubyte3_e32 v155, v87
	v_mul_f32_e32 v206, v124, v108
	v_mul_f32_e32 v207, v125, v108
	v_mul_f32_e32 v208, v140, v108
	v_mul_f32_e32 v209, v141, v108
	v_mul_f32_e32 v156, v126, v109
	v_mul_f32_e32 v157, v127, v109
	v_mul_f32_e32 v158, v142, v109
	v_mul_f32_e32 v159, v143, v109
	v_fmac_f32_e32 v206, v128, v110
	v_fmac_f32_e32 v207, v129, v110
	v_fmac_f32_e32 v208, v144, v110
	v_fmac_f32_e32 v209, v145, v110
	v_fmac_f32_e32 v156, v130, v111
	v_fmac_f32_e32 v157, v131, v111
	v_fmac_f32_e32 v158, v146, v111
	v_fmac_f32_e32 v159, v147, v111
	v_fmac_f32_e32 v206, v132, v112
	v_fmac_f32_e32 v207, v133, v112
	v_fmac_f32_e32 v208, v148, v112
	v_fmac_f32_e32 v209, v149, v112
	v_fmac_f32_e32 v156, v134, v113
	v_fmac_f32_e32 v157, v135, v113
	v_fmac_f32_e32 v158, v150, v113
	v_fmac_f32_e32 v159, v151, v113
	v_fmac_f32_e32 v206, v136, v114
	v_fmac_f32_e32 v207, v137, v114
	v_fmac_f32_e32 v208, v152, v114
	v_fmac_f32_e32 v209, v153, v114
	v_fmac_f32_e32 v156, v138, v115
	v_fmac_f32_e32 v157, v139, v115
	v_fmac_f32_e32 v158, v154, v115
	v_fmac_f32_e32 v159, v155, v115
	v_add_f32_e32 v206, v206, v156
	v_add_f32_e32 v207, v207, v157
	v_add_f32_e32 v208, v208, v158
	v_add_f32_e32 v209, v209, v159
	s_waitcnt lgkmcnt(0)
	s_load_dwordx16 s[84:99], s[38:39], 0x40 glc
	s_lshl_b32 s30, s68, 12
	s_add_u32 s28, s26, s30
	s_addc_u32 s29, s27, 0
	global_load_dwordx2 v[24:25], v162, s[28:29]
	s_lshl_b32 s30, s69, 12
	s_add_u32 s28, s26, s30
	s_addc_u32 s29, s27, 0
	global_load_dwordx2 v[26:27], v162, s[28:29]
	s_lshl_b32 s30, s70, 12
	s_add_u32 s28, s26, s30
	s_addc_u32 s29, s27, 0
	global_load_dwordx2 v[28:29], v162, s[28:29]
	s_lshl_b32 s30, s71, 12
	s_add_u32 s28, s26, s30
	s_addc_u32 s29, s27, 0
	global_load_dwordx2 v[30:31], v162, s[28:29]
	s_lshl_b32 s30, s72, 12
	s_add_u32 s28, s26, s30
	s_addc_u32 s29, s27, 0
	global_load_dwordx2 v[32:33], v162, s[28:29]
	s_lshl_b32 s30, s73, 12
	s_add_u32 s28, s26, s30
	s_addc_u32 s29, s27, 0
	global_load_dwordx2 v[34:35], v162, s[28:29]
	s_lshl_b32 s30, s74, 12
	s_add_u32 s28, s26, s30
	s_addc_u32 s29, s27, 0
	global_load_dwordx2 v[36:37], v162, s[28:29]
	s_lshl_b32 s30, s75, 12
	s_add_u32 s28, s26, s30
	s_addc_u32 s29, s27, 0
	global_load_dwordx2 v[38:39], v162, s[28:29]
	s_lshl_b32 s30, s76, 12
	s_add_u32 s28, s26, s30
	s_addc_u32 s29, s27, 0
	global_load_dwordx2 v[40:41], v162, s[28:29]
	s_lshl_b32 s30, s77, 12
	s_add_u32 s28, s26, s30
	s_addc_u32 s29, s27, 0
	global_load_dwordx2 v[42:43], v162, s[28:29]
	s_lshl_b32 s30, s78, 12
	s_add_u32 s28, s26, s30
	s_addc_u32 s29, s27, 0
	global_load_dwordx2 v[44:45], v162, s[28:29]
	s_lshl_b32 s30, s79, 12
	s_add_u32 s28, s26, s30
	s_addc_u32 s29, s27, 0
	global_load_dwordx2 v[46:47], v162, s[28:29]
	s_lshl_b32 s30, s80, 12
	s_add_u32 s28, s26, s30
	s_addc_u32 s29, s27, 0
	global_load_dwordx2 v[48:49], v162, s[28:29]
	s_lshl_b32 s30, s81, 12
	s_add_u32 s28, s26, s30
	s_addc_u32 s29, s27, 0
	global_load_dwordx2 v[50:51], v162, s[28:29]
	s_lshl_b32 s30, s82, 12
	s_add_u32 s28, s26, s30
	s_addc_u32 s29, s27, 0
	global_load_dwordx2 v[52:53], v162, s[28:29]
	s_lshl_b32 s30, s83, 12
	s_add_u32 s28, s26, s30
	s_addc_u32 s29, s27, 0
	global_load_dwordx2 v[54:55], v162, s[28:29]
	s_waitcnt lgkmcnt(0)
	s_load_dwordx16 s[68:83], s[38:39], 0x80 glc
	s_lshl_b32 s30, s84, 12
	s_add_u32 s28, s26, s30
	s_addc_u32 s29, s27, 0
	global_load_dwordx2 v[56:57], v162, s[28:29]
	s_lshl_b32 s30, s85, 12
	s_add_u32 s28, s26, s30
	s_addc_u32 s29, s27, 0
	global_load_dwordx2 v[58:59], v162, s[28:29]
	s_lshl_b32 s30, s86, 12
	s_add_u32 s28, s26, s30
	s_addc_u32 s29, s27, 0
	global_load_dwordx2 v[60:61], v162, s[28:29]
	s_lshl_b32 s30, s87, 12
	s_add_u32 s28, s26, s30
	s_addc_u32 s29, s27, 0
	global_load_dwordx2 v[62:63], v162, s[28:29]
	s_lshl_b32 s30, s88, 12
	s_add_u32 s28, s26, s30
	s_addc_u32 s29, s27, 0
	global_load_dwordx2 v[64:65], v162, s[28:29]
	s_lshl_b32 s30, s89, 12
	s_add_u32 s28, s26, s30
	s_addc_u32 s29, s27, 0
	global_load_dwordx2 v[66:67], v162, s[28:29]
	s_lshl_b32 s30, s90, 12
	s_add_u32 s28, s26, s30
	s_addc_u32 s29, s27, 0
	global_load_dwordx2 v[68:69], v162, s[28:29]
	s_lshl_b32 s30, s91, 12
	s_add_u32 s28, s26, s30
	s_addc_u32 s29, s27, 0
	global_load_dwordx2 v[70:71], v162, s[28:29]
	s_lshl_b32 s30, s92, 12
	s_add_u32 s28, s26, s30
	s_addc_u32 s29, s27, 0
	global_load_dwordx2 v[72:73], v162, s[28:29]
	s_lshl_b32 s30, s93, 12
	s_add_u32 s28, s26, s30
	s_addc_u32 s29, s27, 0
	global_load_dwordx2 v[74:75], v162, s[28:29]
	s_lshl_b32 s30, s94, 12
	s_add_u32 s28, s26, s30
	s_addc_u32 s29, s27, 0
	global_load_dwordx2 v[76:77], v162, s[28:29]
	s_lshl_b32 s30, s95, 12
	s_add_u32 s28, s26, s30
	s_addc_u32 s29, s27, 0
	global_load_dwordx2 v[78:79], v162, s[28:29]
	s_lshl_b32 s30, s96, 12
	s_add_u32 s28, s26, s30
	s_addc_u32 s29, s27, 0
	global_load_dwordx2 v[80:81], v162, s[28:29]
	s_lshl_b32 s30, s97, 12
	s_add_u32 s28, s26, s30
	s_addc_u32 s29, s27, 0
	global_load_dwordx2 v[82:83], v162, s[28:29]
	s_lshl_b32 s30, s98, 12
	s_add_u32 s28, s26, s30
	s_addc_u32 s29, s27, 0
	global_load_dwordx2 v[84:85], v162, s[28:29]
	s_lshl_b32 s30, s99, 12
	s_add_u32 s28, s26, s30
	s_addc_u32 s29, s27, 0
	global_load_dwordx2 v[86:87], v162, s[28:29]
	v_permlane32_swap_b32_e32 v178, v194
	v_permlane32_swap_b32_e32 v179, v195
	v_permlane32_swap_b32_e32 v180, v196
	v_permlane32_swap_b32_e32 v181, v197
	v_permlane32_swap_b32_e32 v182, v198
	v_permlane32_swap_b32_e32 v183, v199
	v_permlane32_swap_b32_e32 v184, v200
	v_permlane32_swap_b32_e32 v185, v201
	v_permlane32_swap_b32_e32 v186, v202
	v_permlane32_swap_b32_e32 v187, v203
	v_permlane32_swap_b32_e32 v188, v204
	v_permlane32_swap_b32_e32 v189, v205
	v_permlane32_swap_b32_e32 v190, v206
	v_permlane32_swap_b32_e32 v191, v207
	v_permlane32_swap_b32_e32 v192, v208
	v_permlane32_swap_b32_e32 v193, v209
	v_add_f32_e32 v178, v178, v194
	v_add_f32_e32 v179, v179, v195
	v_add_f32_e32 v180, v180, v196
	v_add_f32_e32 v181, v181, v197
	v_add_f32_e32 v182, v182, v198
	v_add_f32_e32 v183, v183, v199
	v_add_f32_e32 v184, v184, v200
	v_add_f32_e32 v185, v185, v201
	v_add_f32_e32 v186, v186, v202
	v_add_f32_e32 v187, v187, v203
	v_add_f32_e32 v188, v188, v204
	v_add_f32_e32 v189, v189, v205
	v_add_f32_e32 v190, v190, v206
	v_add_f32_e32 v191, v191, v207
	v_add_f32_e32 v192, v192, v208
	v_add_f32_e32 v193, v193, v209
	v_permlane16_swap_b32_e32 v178, v186
	v_permlane16_swap_b32_e32 v179, v187
	v_permlane16_swap_b32_e32 v180, v188
	v_permlane16_swap_b32_e32 v181, v189
	v_permlane16_swap_b32_e32 v182, v190
	v_permlane16_swap_b32_e32 v183, v191
	v_permlane16_swap_b32_e32 v184, v192
	v_permlane16_swap_b32_e32 v185, v193
	v_add_f32_e32 v178, v178, v186
	v_add_f32_e32 v179, v179, v187
	v_add_f32_e32 v180, v180, v188
	v_add_f32_e32 v181, v181, v189
	v_add_f32_e32 v182, v182, v190
	v_add_f32_e32 v183, v183, v191
	v_add_f32_e32 v184, v184, v192
	v_add_f32_e32 v185, v185, v193
	v_cndmask_b32_e64 v2, v178, v182, s[8:9]
	v_cndmask_b32_e64 v3, v179, v183, s[8:9]
	v_cndmask_b32_e64 v4, v180, v184, s[8:9]
	v_cndmask_b32_e64 v5, v181, v185, s[8:9]
	v_cndmask_b32_e64 v6, v182, v178, s[8:9]
	v_cndmask_b32_e64 v7, v183, v179, s[8:9]
	v_cndmask_b32_e64 v8, v184, v180, s[8:9]
	v_cndmask_b32_e64 v9, v185, v181, s[8:9]
	v_add_f32_dpp v6, v2, v6 row_ror:8 row_mask:0xf bank_mask:0xf
	v_add_f32_dpp v7, v3, v7 row_ror:8 row_mask:0xf bank_mask:0xf
	v_add_f32_dpp v8, v4, v8 row_ror:8 row_mask:0xf bank_mask:0xf
	v_add_f32_dpp v9, v5, v9 row_ror:8 row_mask:0xf bank_mask:0xf
	v_cndmask_b32_e64 v2, v6, v8, s[10:11]
	v_cndmask_b32_e64 v3, v7, v9, s[10:11]
	v_cndmask_b32_e64 v4, v8, v6, s[10:11]
	v_cndmask_b32_e64 v5, v9, v7, s[10:11]
	v_add_f32_dpp v4, v2, v4 row_half_mirror row_mask:0xf bank_mask:0xf
	v_add_f32_dpp v5, v3, v5 row_half_mirror row_mask:0xf bank_mask:0xf
	v_cndmask_b32_e64 v2, v4, v5, s[14:15]
	v_cndmask_b32_e64 v3, v5, v4, s[14:15]
	s_nop 0
	v_add_f32_dpp v3, v2, v3 quad_perm:[2,3,0,1] row_mask:0xf bank_mask:0xf
	s_nop 1
	v_add_f32_dpp v11, v3, v3 quad_perm:[1,0,3,2] row_mask:0xf bank_mask:0xf
	s_mov_b64 exec, s[2:3]
	global_store_dword v[22:23], v11, off offset:384
	s_mov_b64 exec, -1
	s_add_i32 s16, s16, 1
	s_cmp_lt_i32 s16, s17
	s_cbranch_scc1 .Lpa_tok
	s_waitcnt vmcnt(0)
	s_waitcnt vmcnt(0)
	v_cmp_eq_u32_e32 vcc, 0, v0
	s_waitcnt vmcnt(0) lgkmcnt(0)
	s_barrier
	s_and_saveexec_b64 s[2:3], vcc
	s_cbranch_execz .Lgbb_1444
	v_readlane_b32 s4, v237, 5
	s_waitcnt vmcnt(0) expcnt(0) lgkmcnt(0)
	s_nop 0
	v_mov_b32_e32 v1, s4
	ds_read_b32 v3, v1
	ds_read_b32 v1, v1 offset:4
	s_waitcnt lgkmcnt(1)
	v_cmp_ne_u32_e32 vcc, 0, v3
	s_branch .Lgbb_1412
	v_readlane_b32 s4, v237, 2
	v_readlane_b32 s5, v237, 3
	s_load_dwordx2 s[8:9], s[6:7], 0x4
	s_lshl_b64 s[4:5], s[4:5], 2
	v_readlane_b32 s6, v237, 0
	s_add_u32 s4, s6, s4
	v_readlane_b32 s6, v237, 1
	s_addc_u32 s5, s6, s5
	s_add_u32 s6, s4, 0x1000
	s_addc_u32 s7, s5, 0
	s_waitcnt lgkmcnt(0)
	s_mul_i32 s20, s8, s38
	s_add_u32 s8, s4, 0x1100
	s_mul_i32 s20, s20, s9
	s_addc_u32 s9, s5, 0
	s_add_u32 s10, s4, 0x1200
	s_addc_u32 s11, s5, 0
	s_add_u32 s12, s4, 0x1300
	s_addc_u32 s13, s5, 0
	s_mov_b32 s21, 1
	v_mov_b32_e32 v17, 0
	s_branch .Lgbb_1400
